# topk: static priority raise (s_setprio 2) for the load+MFMA+pack segment of each half, back to 0 for the sort
# speedup vs baseline: 1.0010x; 1.0010x over previous
.LBB0_704:
	s_setprio 2
	v_cndmask_b32_e64 v0, 0, 1, s[6:7]
	s_lshl_b32 s36, s8, 8
	v_cmp_ne_u32_e32 vcc, 1, v0
	v_lshl_add_u64 v[0:1], v[178:179], 0, s[36:37]
	global_load_dwordx4 v[44:47], v[0:1], off
	global_load_dwordx4 v[40:43], v[0:1], off offset:32
	global_load_dwordx4 v[36:39], v[0:1], off offset:64
	global_load_dwordx4 v[32:35], v[0:1], off offset:96
	global_load_dwordx4 v[28:31], v[0:1], off offset:128
	global_load_dwordx4 v[24:27], v[0:1], off offset:160
	global_load_dwordx4 v[20:23], v[0:1], off offset:192
	global_load_dwordx4 v[16:19], v[0:1], off offset:224
	v_lshl_or_b32 v180, s8, 7, v209
	v_ashrrev_i32_e32 v181, 31, v180
	v_lshlrev_b64 v[0:1], 8, v[180:181]
	v_lshl_add_u64 v[60:61], v[64:65], 0, v[0:1]
	global_load_dwordx4 v[0:3], v[60:61], off
	global_load_dwordx4 v[48:51], v[60:61], off offset:32
	global_load_dwordx4 v[52:55], v[60:61], off offset:64
	global_load_dwordx4 v[56:59], v[60:61], off offset:96
	global_load_dwordx4 v[68:71], v[60:61], off offset:128
	global_load_dwordx4 v[72:75], v[60:61], off offset:160
	global_load_dwordx4 v[76:79], v[60:61], off offset:192
	global_load_dwordx4 v[80:83], v[60:61], off offset:224
	s_mov_b32 s12, 0x2000
	s_mov_b32 s13, 0
	v_lshl_add_u64 v[186:187], v[60:61], 0, s[12:13]
	global_load_dwordx4 v[84:87], v[186:187], off
	global_load_dwordx4 v[88:91], v[186:187], off offset:32
	global_load_dwordx4 v[92:95], v[186:187], off offset:64
	global_load_dwordx4 v[96:99], v[186:187], off offset:96
	global_load_dwordx4 v[100:103], v[186:187], off offset:128
	global_load_dwordx4 v[104:107], v[186:187], off offset:160
	global_load_dwordx4 v[108:111], v[186:187], off offset:192
	global_load_dwordx4 v[112:115], v[186:187], off offset:224
	v_lshl_add_u64 v[188:189], v[186:187], 0, s[12:13]
	global_load_dwordx4 v[116:119], v[188:189], off
	global_load_dwordx4 v[120:123], v[188:189], off offset:32
	global_load_dwordx4 v[124:127], v[188:189], off offset:64
	global_load_dwordx4 v[128:131], v[188:189], off offset:96
	global_load_dwordx4 v[132:135], v[188:189], off offset:128
	global_load_dwordx4 v[136:139], v[188:189], off offset:160
	global_load_dwordx4 v[140:143], v[188:189], off offset:192
	global_load_dwordx4 v[152:155], v[188:189], off offset:224
	v_lshl_add_u64 v[186:187], v[188:189], 0, s[12:13]
	global_load_dwordx4 v[156:159], v[186:187], off
	global_load_dwordx4 v[160:163], v[186:187], off offset:32
	global_load_dwordx4 v[164:167], v[186:187], off offset:64
	global_load_dwordx4 v[168:171], v[186:187], off offset:96
	s_waitcnt vmcnt(24)
	v_mfma_f32_32x32x16_bf16 v[0:15], v[0:3], v[44:47], 0
	v_mfma_f32_32x32x16_bf16 v[0:15], v[48:51], v[40:43], v[0:15]
	v_mfma_f32_32x32x16_bf16 v[0:15], v[52:55], v[36:39], v[0:15]
	v_mfma_f32_32x32x16_bf16 v[0:15], v[56:59], v[32:35], v[0:15]
	global_load_dwordx4 v[48:51], v[186:187], off offset:128
	global_load_dwordx4 v[52:55], v[186:187], off offset:160
	global_load_dwordx4 v[56:59], v[186:187], off offset:192
	global_load_dwordx4 v[60:63], v[186:187], off offset:224
	s_waitcnt vmcnt(27)
	v_mfma_f32_32x32x16_bf16 v[0:15], v[68:71], v[28:31], v[0:15]
	s_waitcnt vmcnt(26)
	v_mfma_f32_32x32x16_bf16 v[0:15], v[72:75], v[24:27], v[0:15]
	s_waitcnt vmcnt(25)
	v_mfma_f32_32x32x16_bf16 v[0:15], v[76:79], v[20:23], v[0:15]
	s_waitcnt vmcnt(24)
	v_mfma_f32_32x32x16_bf16 v[0:15], v[80:83], v[16:19], v[0:15]
	v_or_b32_e32 v172, 1, v66
	v_xor_b32_e32 v174, 0x7e, v66
	s_nop 9
	v_cmp_gt_i32_e64 s[6:7], 0, v1
	v_xor_b32_e32 v67, 0x7f, v66
	v_and_b32_e32 v1, 0xffffff80, v1
	v_cndmask_b32_e64 v172, v174, v172, s[6:7]
	v_cmp_gt_i32_e64 s[6:7], 0, v0
	v_and_b32_e32 v0, 0xffffff80, v0
	v_or_b32_e32 v210, v172, v1
	v_cndmask_b32_e64 v67, v67, v66, s[6:7]
	v_or_b32_e32 v211, v67, v0
	v_or_b32_e32 v1, 3, v66
	v_xor_b32_e32 v173, 0x7c, v66
	v_cmp_gt_i32_e64 s[6:7], 0, v3
	v_or_b32_e32 v0, 2, v66
	v_xor_b32_e32 v190, 0x7d, v66
	v_cndmask_b32_e64 v1, v173, v1, s[6:7]
	v_cmp_gt_i32_e64 s[6:7], 0, v2
	v_and_b32_e32 v3, 0xffffff80, v3
	v_and_b32_e32 v2, 0xffffff80, v2
	v_cndmask_b32_e64 v0, v190, v0, s[6:7]
	v_or_b32_e32 v173, v1, v3
	v_or_b32_e32 v1, 9, v66
	v_xor_b32_e32 v3, 0x76, v66
	v_cmp_gt_i32_e64 s[6:7], 0, v5
	v_or_b32_e32 v212, v0, v2
	v_or_b32_e32 v0, 8, v66
	v_cndmask_b32_e64 v1, v3, v1, s[6:7]
	v_xor_b32_e32 v2, 0x77, v66
	v_cmp_gt_i32_e64 s[6:7], 0, v4
	v_and_b32_e32 v3, 0xffffff80, v4
	s_nop 0
	v_cndmask_b32_e64 v0, v2, v0, s[6:7]
	v_and_b32_e32 v2, 0xffffff80, v5
	v_or_b32_e32 v213, v1, v2
	v_or_b32_e32 v214, v0, v3
	v_or_b32_e32 v1, 11, v66
	v_xor_b32_e32 v3, 0x74, v66
	v_cmp_gt_i32_e64 s[6:7], 0, v7
	v_or_b32_e32 v0, 10, v66
	v_xor_b32_e32 v2, 0x75, v66
	v_cndmask_b32_e64 v1, v3, v1, s[6:7]
	v_cmp_gt_i32_e64 s[6:7], 0, v6
	v_and_b32_e32 v3, 0xffffff80, v6
	s_nop 0
	v_cndmask_b32_e64 v0, v2, v0, s[6:7]
	v_and_b32_e32 v2, 0xffffff80, v7
	v_or_b32_e32 v215, v1, v2
	v_or_b32_e32 v216, v0, v3
	v_or_b32_e32 v1, 17, v66
	v_xor_b32_e32 v3, 0x6e, v66
	v_cmp_gt_i32_e64 s[6:7], 0, v9
	v_or_b32_e32 v0, 16, v66
	v_xor_b32_e32 v2, 0x6f, v66
	v_cndmask_b32_e64 v1, v3, v1, s[6:7]
	v_cmp_gt_i32_e64 s[6:7], 0, v8
	v_and_b32_e32 v3, 0xffffff80, v8
	s_nop 0
	v_cndmask_b32_e64 v0, v2, v0, s[6:7]
	v_and_b32_e32 v2, 0xffffff80, v9
	v_or_b32_e32 v217, v1, v2
	v_or_b32_e32 v218, v0, v3
	v_or_b32_e32 v1, 19, v66
	v_xor_b32_e32 v3, 0x6c, v66
	v_cmp_gt_i32_e64 s[6:7], 0, v11
	v_or_b32_e32 v0, 18, v66
	v_xor_b32_e32 v2, 0x6d, v66
	v_cndmask_b32_e64 v1, v3, v1, s[6:7]
	v_cmp_gt_i32_e64 s[6:7], 0, v10
	v_and_b32_e32 v3, 0xffffff80, v10
	s_nop 0
	v_cndmask_b32_e64 v0, v2, v0, s[6:7]
	v_and_b32_e32 v2, 0xffffff80, v11
	v_or_b32_e32 v219, v1, v2
	v_or_b32_e32 v220, v0, v3
	v_or_b32_e32 v1, 25, v66
	v_xor_b32_e32 v3, 0x66, v66
	v_cmp_gt_i32_e64 s[6:7], 0, v13
	v_or_b32_e32 v0, 24, v66
	v_xor_b32_e32 v2, 0x67, v66
	v_cndmask_b32_e64 v1, v3, v1, s[6:7]
	v_cmp_gt_i32_e64 s[6:7], 0, v12
	v_and_b32_e32 v3, 0xffffff80, v12
	s_nop 0
	v_cndmask_b32_e64 v0, v2, v0, s[6:7]
	v_and_b32_e32 v2, 0xffffff80, v13
	v_or_b32_e32 v221, v1, v2
	v_or_b32_e32 v1, 27, v66
	v_cmp_gt_i32_e64 s[6:7], 0, v15
	v_or_b32_e32 v222, v0, v3
	v_and_b32_e32 v2, 0xffffff80, v15
	v_xor_b32_e32 v0, 0x64, v66
	v_cndmask_b32_e64 v0, v0, v1, s[6:7]
	v_cmp_gt_i32_e64 s[6:7], 0, v14
	v_and_b32_e32 v3, 0xffffff80, v14
	v_or_b32_e32 v223, v0, v2
	v_xor_b32_e32 v1, 0x65, v66
	v_or_b32_e32 v188, 26, v66
	v_cndmask_b32_e64 v1, v1, v188, s[6:7]
	v_or_b32_e32 v224, v1, v3
	s_waitcnt vmcnt(23)
	v_mfma_f32_32x32x16_bf16 v[0:15], v[84:87], v[44:47], 0
	s_waitcnt vmcnt(22)
	v_mfma_f32_32x32x16_bf16 v[0:15], v[88:91], v[40:43], v[0:15]
	s_waitcnt vmcnt(21)
	v_mfma_f32_32x32x16_bf16 v[0:15], v[92:95], v[36:39], v[0:15]
	s_waitcnt vmcnt(20)
	v_mfma_f32_32x32x16_bf16 v[0:15], v[96:99], v[32:35], v[0:15]
	s_waitcnt vmcnt(19)
	v_mfma_f32_32x32x16_bf16 v[0:15], v[100:103], v[28:31], v[0:15]
	s_waitcnt vmcnt(18)
	v_mfma_f32_32x32x16_bf16 v[0:15], v[104:107], v[24:27], v[0:15]
	s_waitcnt vmcnt(17)
	v_mfma_f32_32x32x16_bf16 v[0:15], v[108:111], v[20:23], v[0:15]
	s_waitcnt vmcnt(16)
	v_mfma_f32_32x32x16_bf16 v[0:15], v[112:115], v[16:19], v[0:15]
	s_nop 3
	s_nop 7
	v_cmp_gt_i32_e64 s[6:7], 0, v1
	v_and_b32_e32 v1, 0xffffff80, v1
	v_xor_b32_e32 v181, 0x5e, v66
	v_or_b32_e32 v188, 33, v66
	v_cndmask_b32_e64 v181, v181, v188, s[6:7]
	v_cmp_gt_i32_e64 s[6:7], 0, v0
	v_and_b32_e32 v0, 0xffffff80, v0
	v_or_b32_e32 v225, v181, v1
	v_xor_b32_e32 v190, 0x5f, v66
	v_or_b32_e32 v188, 32, v66
	v_cndmask_b32_e64 v190, v190, v188, s[6:7]
	v_cmp_gt_i32_e64 s[6:7], 0, v3
	v_or_b32_e32 v226, v190, v0
	v_and_b32_e32 v3, 0xffffff80, v3
	v_xor_b32_e32 v0, 0x5c, v66
	v_or_b32_e32 v188, 35, v66
	v_cndmask_b32_e64 v0, v0, v188, s[6:7]
	v_cmp_gt_i32_e64 s[6:7], 0, v2
	v_and_b32_e32 v2, 0xffffff80, v2
	v_or_b32_e32 v227, v0, v3
	v_xor_b32_e32 v1, 0x5d, v66
	v_or_b32_e32 v188, 34, v66
	v_cndmask_b32_e64 v1, v1, v188, s[6:7]
	v_cmp_gt_i32_e64 s[6:7], 0, v5
	v_or_b32_e32 v228, v1, v2
	v_and_b32_e32 v2, 0xffffff80, v5
	v_xor_b32_e32 v0, 0x56, v66
	v_or_b32_e32 v188, 41, v66
	v_cndmask_b32_e64 v0, v0, v188, s[6:7]
	v_cmp_gt_i32_e64 s[6:7], 0, v4
	v_and_b32_e32 v3, 0xffffff80, v4
	v_or_b32_e32 v229, v0, v2
	v_xor_b32_e32 v1, 0x57, v66
	v_or_b32_e32 v188, 40, v66
	v_cndmask_b32_e64 v1, v1, v188, s[6:7]
	v_cmp_gt_i32_e64 s[6:7], 0, v7
	v_or_b32_e32 v230, v1, v3
	v_and_b32_e32 v2, 0xffffff80, v7
	v_xor_b32_e32 v0, 0x54, v66
	v_or_b32_e32 v188, 43, v66
	v_cndmask_b32_e64 v0, v0, v188, s[6:7]
	v_cmp_gt_i32_e64 s[6:7], 0, v6
	v_and_b32_e32 v3, 0xffffff80, v6
	v_or_b32_e32 v231, v0, v2
	v_xor_b32_e32 v1, 0x55, v66
	v_or_b32_e32 v188, 42, v66
	v_cndmask_b32_e64 v1, v1, v188, s[6:7]
	v_cmp_gt_i32_e64 s[6:7], 0, v9
	v_or_b32_e32 v232, v1, v3
	v_and_b32_e32 v2, 0xffffff80, v9
	v_xor_b32_e32 v0, 0x4e, v66
	v_or_b32_e32 v188, 49, v66
	v_cndmask_b32_e64 v0, v0, v188, s[6:7]
	v_cmp_gt_i32_e64 s[6:7], 0, v8
	v_and_b32_e32 v3, 0xffffff80, v8
	v_or_b32_e32 v233, v0, v2
	v_xor_b32_e32 v1, 0x4f, v66
	v_or_b32_e32 v188, 48, v66
	v_cndmask_b32_e64 v1, v1, v188, s[6:7]
	v_cmp_gt_i32_e64 s[6:7], 0, v11
	v_or_b32_e32 v234, v1, v3
	v_and_b32_e32 v2, 0xffffff80, v11
	v_xor_b32_e32 v0, 0x4c, v66
	v_or_b32_e32 v188, 51, v66
	v_cndmask_b32_e64 v0, v0, v188, s[6:7]
	v_cmp_gt_i32_e64 s[6:7], 0, v10
	v_and_b32_e32 v3, 0xffffff80, v10
	v_or_b32_e32 v235, v0, v2
	v_xor_b32_e32 v1, 0x4d, v66
	v_or_b32_e32 v188, 50, v66
	v_cndmask_b32_e64 v1, v1, v188, s[6:7]
	v_cmp_gt_i32_e64 s[6:7], 0, v13
	v_or_b32_e32 v236, v1, v3
	v_and_b32_e32 v2, 0xffffff80, v13
	v_xor_b32_e32 v0, 0x46, v66
	v_or_b32_e32 v188, 57, v66
	v_cndmask_b32_e64 v0, v0, v188, s[6:7]
	v_cmp_gt_i32_e64 s[6:7], 0, v12
	v_and_b32_e32 v3, 0xffffff80, v12
	v_or_b32_e32 v237, v0, v2
	v_xor_b32_e32 v1, 0x47, v66
	v_or_b32_e32 v188, 56, v66
	v_cndmask_b32_e64 v1, v1, v188, s[6:7]
	v_cmp_gt_i32_e64 s[6:7], 0, v15
	v_or_b32_e32 v238, v1, v3
	v_and_b32_e32 v2, 0xffffff80, v15
	v_xor_b32_e32 v0, 0x44, v66
	v_or_b32_e32 v188, 59, v66
	v_cndmask_b32_e64 v0, v0, v188, s[6:7]
	v_cmp_gt_i32_e64 s[6:7], 0, v14
	v_and_b32_e32 v3, 0xffffff80, v14
	v_or_b32_e32 v239, v0, v2
	v_xor_b32_e32 v1, 0x45, v66
	v_or_b32_e32 v188, 58, v66
	v_cndmask_b32_e64 v1, v1, v188, s[6:7]
	v_or_b32_e32 v240, v1, v3
	s_waitcnt vmcnt(15)
	v_mfma_f32_32x32x16_bf16 v[0:15], v[116:119], v[44:47], 0
	s_waitcnt vmcnt(14)
	v_mfma_f32_32x32x16_bf16 v[0:15], v[120:123], v[40:43], v[0:15]
	s_waitcnt vmcnt(13)
	v_mfma_f32_32x32x16_bf16 v[0:15], v[124:127], v[36:39], v[0:15]
	s_waitcnt vmcnt(12)
	v_mfma_f32_32x32x16_bf16 v[0:15], v[128:131], v[32:35], v[0:15]
	s_waitcnt vmcnt(11)
	v_mfma_f32_32x32x16_bf16 v[0:15], v[132:135], v[28:31], v[0:15]
	s_waitcnt vmcnt(10)
	v_mfma_f32_32x32x16_bf16 v[0:15], v[136:139], v[24:27], v[0:15]
	s_waitcnt vmcnt(9)
	v_mfma_f32_32x32x16_bf16 v[0:15], v[140:143], v[20:23], v[0:15]
	s_waitcnt vmcnt(8)
	v_mfma_f32_32x32x16_bf16 v[0:15], v[152:155], v[16:19], v[0:15]
	s_nop 3
	s_nop 7
	v_cmp_gt_i32_e64 s[6:7], 0, v1
	v_and_b32_e32 v1, 0xffffff80, v1
	v_xor_b32_e32 v182, 62, v66
	v_or_b32_e32 v188, 0x41, v66
	v_cndmask_b32_e64 v182, v182, v188, s[6:7]
	v_cmp_gt_i32_e64 s[6:7], 0, v0
	v_and_b32_e32 v0, 0xffffff80, v0
	v_or_b32_e32 v182, v182, v1
	v_xor_b32_e32 v183, 63, v66
	v_or_b32_e32 v188, 64, v66
	v_cndmask_b32_e64 v183, v183, v188, s[6:7]
	v_cmp_gt_i32_e64 s[6:7], 0, v3
	v_or_b32_e32 v183, v183, v0
	v_and_b32_e32 v3, 0xffffff80, v3
	v_xor_b32_e32 v0, 60, v66
	v_or_b32_e32 v188, 0x43, v66
	v_cndmask_b32_e64 v0, v0, v188, s[6:7]
	v_cmp_gt_i32_e64 s[6:7], 0, v2
	v_and_b32_e32 v2, 0xffffff80, v2
	v_or_b32_e32 v241, v0, v3
	v_xor_b32_e32 v1, 61, v66
	v_or_b32_e32 v188, 0x42, v66
	v_cndmask_b32_e64 v1, v1, v188, s[6:7]
	v_cmp_gt_i32_e64 s[6:7], 0, v5
	v_or_b32_e32 v242, v1, v2
	v_and_b32_e32 v2, 0xffffff80, v5
	v_xor_b32_e32 v0, 54, v66
	v_or_b32_e32 v188, 0x49, v66
	v_cndmask_b32_e64 v0, v0, v188, s[6:7]
	v_cmp_gt_i32_e64 s[6:7], 0, v4
	v_and_b32_e32 v3, 0xffffff80, v4
	v_or_b32_e32 v243, v0, v2
	v_xor_b32_e32 v1, 55, v66
	v_or_b32_e32 v188, 0x48, v66
	v_cndmask_b32_e64 v1, v1, v188, s[6:7]
	v_cmp_gt_i32_e64 s[6:7], 0, v7
	v_or_b32_e32 v244, v1, v3
	v_and_b32_e32 v2, 0xffffff80, v7
	v_xor_b32_e32 v0, 52, v66
	v_or_b32_e32 v188, 0x4b, v66
	v_cndmask_b32_e64 v0, v0, v188, s[6:7]
	v_cmp_gt_i32_e64 s[6:7], 0, v6
	v_and_b32_e32 v3, 0xffffff80, v6
	v_or_b32_e32 v245, v0, v2
	v_xor_b32_e32 v1, 53, v66
	v_or_b32_e32 v188, 0x4a, v66
	v_cndmask_b32_e64 v1, v1, v188, s[6:7]
	v_cmp_gt_i32_e64 s[6:7], 0, v9
	v_or_b32_e32 v246, v1, v3
	v_and_b32_e32 v2, 0xffffff80, v9
	v_xor_b32_e32 v0, 46, v66
	v_or_b32_e32 v188, 0x51, v66
	v_cndmask_b32_e64 v0, v0, v188, s[6:7]
	v_cmp_gt_i32_e64 s[6:7], 0, v8
	v_and_b32_e32 v3, 0xffffff80, v8
	v_or_b32_e32 v247, v0, v2
	v_xor_b32_e32 v1, 47, v66
	v_or_b32_e32 v188, 0x50, v66
	v_cndmask_b32_e64 v1, v1, v188, s[6:7]
	v_cmp_gt_i32_e64 s[6:7], 0, v11
	v_or_b32_e32 v248, v1, v3
	v_and_b32_e32 v2, 0xffffff80, v11
	v_xor_b32_e32 v0, 44, v66
	v_or_b32_e32 v188, 0x53, v66
	v_cndmask_b32_e64 v0, v0, v188, s[6:7]
	v_cmp_gt_i32_e64 s[6:7], 0, v10
	v_and_b32_e32 v3, 0xffffff80, v10
	v_or_b32_e32 v249, v0, v2
	v_xor_b32_e32 v1, 45, v66
	v_or_b32_e32 v188, 0x52, v66
	v_cndmask_b32_e64 v1, v1, v188, s[6:7]
	v_cmp_gt_i32_e64 s[6:7], 0, v13
	v_or_b32_e32 v250, v1, v3
	v_and_b32_e32 v2, 0xffffff80, v13
	v_xor_b32_e32 v0, 38, v66
	v_or_b32_e32 v188, 0x59, v66
	v_cndmask_b32_e64 v0, v0, v188, s[6:7]
	v_cmp_gt_i32_e64 s[6:7], 0, v12
	v_and_b32_e32 v3, 0xffffff80, v12
	v_or_b32_e32 v251, v0, v2
	v_xor_b32_e32 v1, 39, v66
	v_or_b32_e32 v188, 0x58, v66
	v_cndmask_b32_e64 v1, v1, v188, s[6:7]
	v_cmp_gt_i32_e64 s[6:7], 0, v15
	v_or_b32_e32 v252, v1, v3
	v_and_b32_e32 v2, 0xffffff80, v15
	v_xor_b32_e32 v0, 36, v66
	v_or_b32_e32 v188, 0x5b, v66
	v_cndmask_b32_e64 v0, v0, v188, s[6:7]
	v_cmp_gt_i32_e64 s[6:7], 0, v14
	v_and_b32_e32 v3, 0xffffff80, v14
	v_or_b32_e32 v190, v0, v2
	v_xor_b32_e32 v1, 37, v66
	v_or_b32_e32 v188, 0x5a, v66
	v_cndmask_b32_e64 v1, v1, v188, s[6:7]
	v_or_b32_e32 v195, v1, v3
	s_waitcnt vmcnt(7)
	v_mfma_f32_32x32x16_bf16 v[0:15], v[156:159], v[44:47], 0
	s_waitcnt vmcnt(6)
	v_mfma_f32_32x32x16_bf16 v[0:15], v[160:163], v[40:43], v[0:15]
	s_waitcnt vmcnt(5)
	v_mfma_f32_32x32x16_bf16 v[0:15], v[164:167], v[36:39], v[0:15]
	s_waitcnt vmcnt(4)
	v_mfma_f32_32x32x16_bf16 v[0:15], v[168:171], v[32:35], v[0:15]
	s_waitcnt vmcnt(3)
	v_mfma_f32_32x32x16_bf16 v[0:15], v[48:51], v[28:31], v[0:15]
	s_waitcnt vmcnt(2)
	v_mfma_f32_32x32x16_bf16 v[0:15], v[52:55], v[24:27], v[0:15]
	s_waitcnt vmcnt(1)
	v_mfma_f32_32x32x16_bf16 v[0:15], v[56:59], v[20:23], v[0:15]
	s_waitcnt vmcnt(0)
	v_mfma_f32_32x32x16_bf16 v[0:15], v[60:63], v[16:19], v[0:15]
	s_nop 11
	v_cmp_gt_i32_e64 s[6:7], 0, v1
	v_and_b32_e32 v1, 0xffffff80, v1
	v_and_b32_e32 v18, 0xffffff80, v0
	v_xor_b32_e32 v16, 30, v66
	v_or_b32_e32 v188, 0x61, v66
	v_cndmask_b32_e64 v16, v16, v188, s[6:7]
	v_cmp_gt_i32_e64 s[6:7], 0, v0
	v_or_b32_e32 v0, v16, v1
	v_xor_b32_e32 v17, 31, v66
	v_or_b32_e32 v188, 0x60, v66
	v_cndmask_b32_e64 v17, v17, v188, s[6:7]
	v_cmp_gt_i32_e64 s[6:7], 0, v3
	v_or_b32_e32 v1, v17, v18
	v_and_b32_e32 v3, 0xffffff80, v3
	v_xor_b32_e32 v16, 28, v66
	v_or_b32_e32 v188, 0x63, v66
	v_cndmask_b32_e64 v16, v16, v188, s[6:7]
	v_cmp_gt_i32_e64 s[6:7], 0, v2
	v_and_b32_e32 v18, 0xffffff80, v2
	v_or_b32_e32 v2, v16, v3
	v_xor_b32_e32 v17, 29, v66
	v_or_b32_e32 v188, 0x62, v66
	v_cndmask_b32_e64 v17, v17, v188, s[6:7]
	v_cmp_gt_i32_e64 s[6:7], 0, v5
	v_or_b32_e32 v3, v17, v18
	v_and_b32_e32 v5, 0xffffff80, v5
	v_xor_b32_e32 v16, 22, v66
	v_or_b32_e32 v188, 0x69, v66
	v_cndmask_b32_e64 v16, v16, v188, s[6:7]
	v_cmp_gt_i32_e64 s[6:7], 0, v4
	v_and_b32_e32 v18, 0xffffff80, v4
	v_or_b32_e32 v4, v16, v5
	v_xor_b32_e32 v17, 23, v66
	v_or_b32_e32 v188, 0x68, v66
	v_cndmask_b32_e64 v17, v17, v188, s[6:7]
	v_cmp_gt_i32_e64 s[6:7], 0, v7
	v_or_b32_e32 v5, v17, v18
	v_and_b32_e32 v7, 0xffffff80, v7
	v_xor_b32_e32 v16, 20, v66
	v_or_b32_e32 v188, 0x6b, v66
	v_cndmask_b32_e64 v16, v16, v188, s[6:7]
	v_cmp_gt_i32_e64 s[6:7], 0, v6
	v_and_b32_e32 v18, 0xffffff80, v6
	v_or_b32_e32 v6, v16, v7
	v_xor_b32_e32 v17, 21, v66
	v_or_b32_e32 v188, 0x6a, v66
	v_cndmask_b32_e64 v17, v17, v188, s[6:7]
	v_cmp_gt_i32_e64 s[6:7], 0, v9
	v_or_b32_e32 v7, v17, v18
	v_and_b32_e32 v9, 0xffffff80, v9
	v_xor_b32_e32 v16, 14, v66
	v_or_b32_e32 v188, 0x71, v66
	v_cndmask_b32_e64 v16, v16, v188, s[6:7]
	v_cmp_gt_i32_e64 s[6:7], 0, v8
	v_and_b32_e32 v18, 0xffffff80, v8
	v_or_b32_e32 v8, v16, v9
	v_xor_b32_e32 v17, 15, v66
	v_or_b32_e32 v188, 0x70, v66
	v_cndmask_b32_e64 v17, v17, v188, s[6:7]
	v_cmp_gt_i32_e64 s[6:7], 0, v11
	v_or_b32_e32 v9, v17, v18
	v_and_b32_e32 v11, 0xffffff80, v11
	v_xor_b32_e32 v16, 12, v66
	v_or_b32_e32 v188, 0x73, v66
	v_cndmask_b32_e64 v16, v16, v188, s[6:7]
	v_cmp_gt_i32_e64 s[6:7], 0, v10
	v_and_b32_e32 v18, 0xffffff80, v10
	v_or_b32_e32 v10, v16, v11
	v_xor_b32_e32 v17, 13, v66
	v_or_b32_e32 v188, 0x72, v66
	v_cndmask_b32_e64 v17, v17, v188, s[6:7]
	v_cmp_gt_i32_e64 s[6:7], 0, v13
	v_or_b32_e32 v11, v17, v18
	v_and_b32_e32 v13, 0xffffff80, v13
	v_xor_b32_e32 v16, 6, v66
	v_or_b32_e32 v188, 0x79, v66
	v_cndmask_b32_e64 v16, v16, v188, s[6:7]
	v_cmp_gt_i32_e64 s[6:7], 0, v12
	v_and_b32_e32 v18, 0xffffff80, v12
	v_or_b32_e32 v12, v16, v13
	v_xor_b32_e32 v17, 7, v66
	v_or_b32_e32 v188, 0x78, v66
	v_cndmask_b32_e64 v17, v17, v188, s[6:7]
	v_cmp_gt_i32_e64 s[6:7], 0, v15
	v_or_b32_e32 v16, v17, v18
	v_and_b32_e32 v15, 0xffffff80, v15
	v_xor_b32_e32 v13, 4, v66
	v_or_b32_e32 v188, 0x7b, v66
	v_cndmask_b32_e64 v13, v13, v188, s[6:7]
	v_cmp_gt_i32_e64 s[6:7], 0, v14
	v_and_b32_e32 v14, 0xffffff80, v14
	v_or_b32_e32 v25, v13, v15
	v_xor_b32_e32 v17, 5, v66
	v_or_b32_e32 v188, 0x7a, v66
	v_cndmask_b32_e64 v17, v17, v188, s[6:7]
	v_or_b32_e32 v28, v17, v14
	s_setprio 0
	v_max_f32_e32 v13, v211, v221
	v_min_f32_e32 v221, v211, v221
	v_max_f32_e32 v14, v210, v222
	v_min_f32_e32 v222, v210, v222
	v_max_f32_e32 v15, v212, v223
	v_min_f32_e32 v223, v212, v223
	v_max_f32_e32 v17, v173, v224
	v_min_f32_e32 v224, v173, v224
	v_max_f32_e32 v18, v214, v218
	v_min_f32_e32 v218, v214, v218
	v_max_f32_e32 v19, v213, v216
	v_min_f32_e32 v216, v213, v216
	v_max_f32_e32 v20, v215, v219
	v_min_f32_e32 v219, v215, v219
	v_max_f32_e32 v21, v217, v220
	v_min_f32_e32 v220, v217, v220
	v_max_f32_e32 v22, v13, v19
	v_min_f32_e32 v19, v13, v19
	v_max_f32_e32 v23, v14, v20
	v_min_f32_e32 v20, v14, v20
	v_max_f32_e32 v24, v15, v21
	v_min_f32_e32 v21, v15, v21
	v_max_f32_e32 v26, v17, v18
	v_min_f32_e32 v18, v17, v18
	v_max_f32_e32 v27, v216, v221
	v_min_f32_e32 v221, v216, v221
	v_max_f32_e32 v29, v218, v224
	v_min_f32_e32 v224, v218, v224
	v_max_f32_e32 v30, v220, v223
	v_min_f32_e32 v223, v220, v223
	v_max_f32_e32 v31, v219, v222
	v_min_f32_e32 v222, v219, v222
	v_max_f32_e32 v32, v22, v23
	v_min_f32_e32 v23, v22, v23
	v_max_f32_e32 v33, v24, v26
	v_min_f32_e32 v26, v24, v26
	v_max_f32_e32 v34, v18, v19
	v_min_f32_e32 v19, v18, v19
	v_max_f32_e32 v35, v27, v29
	v_min_f32_e32 v29, v27, v29
	v_max_f32_e32 v36, v20, v21
	v_min_f32_e32 v21, v20, v21
	v_max_f32_e32 v37, v30, v31
	v_min_f32_e32 v31, v30, v31
	v_max_f32_e32 v38, v222, v221
	v_min_f32_e32 v221, v222, v221
	v_max_f32_e32 v39, v224, v223
	v_min_f32_e32 v223, v224, v223
	v_max_f32_e32 v40, v32, v33
	v_min_f32_e32 v33, v32, v33
	v_max_f32_e32 v41, v23, v26
	v_min_f32_e32 v26, v23, v26
	v_max_f32_e32 v42, v34, v37
	v_min_f32_e32 v37, v34, v37
	v_max_f32_e32 v43, v19, v31
	v_min_f32_e32 v31, v19, v31
	v_max_f32_e32 v44, v35, v36
	v_min_f32_e32 v36, v35, v36
	v_max_f32_e32 v45, v29, v21
	v_min_f32_e32 v21, v29, v21
	v_max_f32_e32 v46, v38, v39
	v_min_f32_e32 v39, v38, v39
	v_max_f32_e32 v47, v221, v223
	v_min_f32_e32 v223, v221, v223
	v_max_f32_e32 v48, v41, v33
	v_min_f32_e32 v33, v41, v33
	v_max_f32_e32 v49, v26, v46
	v_min_f32_e32 v46, v26, v46
	v_max_f32_e32 v50, v42, v44
	v_min_f32_e32 v44, v42, v44
	v_max_f32_e32 v51, v43, v36
	v_min_f32_e32 v36, v43, v36
	v_max_f32_e32 v52, v45, v37
	v_min_f32_e32 v37, v45, v37
	v_max_f32_e32 v53, v21, v31
	v_min_f32_e32 v31, v21, v31
	v_max_f32_e32 v54, v47, v39
	v_min_f32_e32 v39, v47, v39
	v_max_f32_e32 v55, v48, v50
	v_min_f32_e32 v50, v48, v50
	v_max_f32_e32 v56, v33, v44
	v_min_f32_e32 v44, v33, v44
	v_max_f32_e32 v57, v51, v52
	v_min_f32_e32 v52, v51, v52
	v_max_f32_e32 v58, v36, v37
	v_min_f32_e32 v37, v36, v37
	v_max_f32_e32 v59, v53, v54
	v_min_f32_e32 v54, v53, v54
	v_max_f32_e32 v60, v31, v39
	v_min_f32_e32 v39, v31, v39
	v_max_f32_e32 v61, v56, v50
	v_min_f32_e32 v50, v56, v50
	v_max_f32_e32 v62, v49, v44
	v_min_f32_e32 v44, v49, v44
	v_max_f32_e32 v63, v59, v46
	v_min_f32_e32 v46, v59, v46
	v_max_f32_e32 v211, v60, v54
	v_min_f32_e32 v54, v60, v54
	v_max_f32_e32 v210, v62, v57
	v_min_f32_e32 v57, v62, v57
	v_max_f32_e32 v212, v44, v52
	v_min_f32_e32 v52, v44, v52
	v_max_f32_e32 v173, v58, v63
	v_min_f32_e32 v63, v58, v63
	v_max_f32_e32 v214, v37, v46
	v_min_f32_e32 v46, v37, v46
	v_max_f32_e32 v213, v210, v50
	v_min_f32_e32 v50, v210, v50
	v_max_f32_e32 v215, v57, v212
	v_min_f32_e32 v212, v57, v212
	v_max_f32_e32 v217, v173, v52
	v_min_f32_e32 v52, v173, v52
	v_max_f32_e32 v13, v63, v214
	v_min_f32_e32 v214, v63, v214
	v_max_f32_e32 v14, v211, v46
	v_min_f32_e32 v46, v211, v46
	v_max_f32_e32 v15, v212, v217
	v_min_f32_e32 v217, v212, v217
	v_max_f32_e32 v17, v52, v13
	v_min_f32_e32 v13, v52, v13
	v_max_f32_e32 v216, v226, v237
	v_min_f32_e32 v237, v226, v237
	v_max_f32_e32 v218, v225, v238
	v_min_f32_e32 v238, v225, v238
	v_max_f32_e32 v220, v228, v239
	v_min_f32_e32 v239, v228, v239
	v_max_f32_e32 v219, v227, v240
	v_min_f32_e32 v240, v227, v240
	v_max_f32_e32 v22, v230, v234
	v_min_f32_e32 v234, v230, v234
	v_max_f32_e32 v24, v229, v232
	v_min_f32_e32 v232, v229, v232
	v_max_f32_e32 v18, v231, v235
	v_min_f32_e32 v235, v231, v235
	v_max_f32_e32 v27, v233, v236
	v_min_f32_e32 v236, v233, v236
	v_max_f32_e32 v20, v216, v24
	v_min_f32_e32 v24, v216, v24
	v_max_f32_e32 v30, v218, v18
	v_min_f32_e32 v18, v218, v18
	v_max_f32_e32 v222, v220, v27
	v_min_f32_e32 v27, v220, v27
	v_max_f32_e32 v224, v219, v22
	v_min_f32_e32 v22, v219, v22
	v_max_f32_e32 v32, v232, v237
	v_min_f32_e32 v237, v232, v237
	v_max_f32_e32 v23, v234, v240
	v_min_f32_e32 v240, v234, v240
	v_max_f32_e32 v34, v236, v239
	v_min_f32_e32 v239, v236, v239
	v_max_f32_e32 v19, v235, v238
	v_min_f32_e32 v238, v235, v238
	v_max_f32_e32 v35, v20, v30
	v_min_f32_e32 v30, v20, v30
	v_max_f32_e32 v29, v222, v224
	v_min_f32_e32 v224, v222, v224
	v_max_f32_e32 v38, v22, v24
	v_min_f32_e32 v24, v22, v24
	v_max_f32_e32 v221, v32, v23
	v_min_f32_e32 v23, v32, v23
	v_max_f32_e32 v41, v18, v27
	v_min_f32_e32 v27, v18, v27
	v_max_f32_e32 v26, v34, v19
	v_min_f32_e32 v19, v34, v19
	v_max_f32_e32 v42, v238, v237
	v_min_f32_e32 v237, v238, v237
	v_max_f32_e32 v43, v240, v239
	v_min_f32_e32 v239, v240, v239
	v_max_f32_e32 v45, v35, v29
	v_min_f32_e32 v29, v35, v29
	v_max_f32_e32 v21, v30, v224
	v_min_f32_e32 v224, v30, v224
	v_max_f32_e32 v47, v38, v26
	v_min_f32_e32 v26, v38, v26
	v_max_f32_e32 v48, v24, v19
	v_min_f32_e32 v19, v24, v19
	v_max_f32_e32 v33, v221, v41
	v_min_f32_e32 v41, v221, v41
	v_max_f32_e32 v51, v23, v27
	v_min_f32_e32 v27, v23, v27
	v_max_f32_e32 v36, v42, v43
	v_min_f32_e32 v43, v42, v43
	v_max_f32_e32 v53, v237, v239
	v_min_f32_e32 v239, v237, v239
	v_max_f32_e32 v31, v21, v29
	v_min_f32_e32 v29, v21, v29
	v_max_f32_e32 v56, v224, v36
	v_min_f32_e32 v36, v224, v36
	v_max_f32_e32 v49, v47, v33
	v_min_f32_e32 v33, v47, v33
	v_max_f32_e32 v59, v48, v41
	v_min_f32_e32 v41, v48, v41
	v_max_f32_e32 v60, v51, v26
	v_min_f32_e32 v26, v51, v26
	v_max_f32_e32 v62, v27, v19
	v_min_f32_e32 v19, v27, v19
	v_max_f32_e32 v44, v53, v43
	v_min_f32_e32 v43, v53, v43
	v_max_f32_e32 v58, v31, v49
	v_min_f32_e32 v49, v31, v49
	v_max_f32_e32 v37, v29, v33
	v_min_f32_e32 v33, v29, v33
	v_max_f32_e32 v210, v59, v60
	v_min_f32_e32 v60, v59, v60
	v_max_f32_e32 v57, v41, v26
	v_min_f32_e32 v26, v41, v26
	v_max_f32_e32 v173, v62, v44
	v_min_f32_e32 v44, v62, v44
	v_max_f32_e32 v63, v19, v43
	v_min_f32_e32 v43, v19, v43
	v_max_f32_e32 v211, v37, v49
	v_min_f32_e32 v49, v37, v49
	v_max_f32_e32 v212, v56, v33
	v_min_f32_e32 v33, v56, v33
	v_max_f32_e32 v52, v173, v36
	v_min_f32_e32 v36, v173, v36
	v_max_f32_e32 v226, v63, v44
	v_min_f32_e32 v44, v63, v44
	v_max_f32_e32 v225, v212, v210
	v_min_f32_e32 v210, v212, v210
	v_max_f32_e32 v228, v33, v60
	v_min_f32_e32 v60, v33, v60
	v_max_f32_e32 v227, v57, v52
	v_min_f32_e32 v52, v57, v52
	v_max_f32_e32 v230, v26, v36
	v_min_f32_e32 v36, v26, v36
	v_max_f32_e32 v229, v225, v49
	v_min_f32_e32 v49, v225, v49
	v_max_f32_e32 v231, v210, v228
	v_min_f32_e32 v228, v210, v228
	v_max_f32_e32 v233, v227, v60
	v_min_f32_e32 v60, v227, v60
	v_max_f32_e32 v216, v52, v230
	v_min_f32_e32 v230, v52, v230
	v_max_f32_e32 v218, v226, v36
	v_min_f32_e32 v36, v226, v36
	v_max_f32_e32 v220, v228, v233
	v_min_f32_e32 v233, v228, v233
	v_max_f32_e32 v219, v60, v216
	v_min_f32_e32 v216, v60, v216
	v_max_f32_e32 v232, v183, v251
	v_min_f32_e32 v251, v183, v251
	v_max_f32_e32 v234, v182, v252
	v_min_f32_e32 v252, v182, v252
	v_max_f32_e32 v236, v242, v190
	v_min_f32_e32 v190, v242, v190
	v_max_f32_e32 v235, v241, v195
	v_min_f32_e32 v195, v241, v195
	v_max_f32_e32 v20, v244, v248
	v_min_f32_e32 v248, v244, v248
	v_max_f32_e32 v222, v243, v246
	v_min_f32_e32 v246, v243, v246
	v_max_f32_e32 v22, v245, v249
	v_min_f32_e32 v249, v245, v249
	v_max_f32_e32 v32, v247, v250
	v_min_f32_e32 v250, v247, v250
	v_max_f32_e32 v18, v232, v222
	v_min_f32_e32 v222, v232, v222
	v_max_f32_e32 v34, v234, v22
	v_min_f32_e32 v22, v234, v22
	v_max_f32_e32 v238, v236, v32
	v_min_f32_e32 v32, v236, v32
	v_max_f32_e32 v240, v235, v20
	v_min_f32_e32 v20, v235, v20
	v_max_f32_e32 v35, v246, v251
	v_min_f32_e32 v251, v246, v251
	v_max_f32_e32 v30, v248, v195
	v_min_f32_e32 v195, v248, v195
	v_max_f32_e32 v38, v250, v190
	v_min_f32_e32 v190, v250, v190
	v_max_f32_e32 v24, v249, v252
	v_min_f32_e32 v252, v249, v252
	v_max_f32_e32 v221, v18, v34
	v_min_f32_e32 v34, v18, v34
	v_max_f32_e32 v23, v238, v240
	v_min_f32_e32 v240, v238, v240
	v_max_f32_e32 v42, v20, v222
	v_min_f32_e32 v222, v20, v222
	v_max_f32_e32 v237, v35, v30
	v_min_f32_e32 v30, v35, v30
	v_max_f32_e32 v21, v22, v32
	v_min_f32_e32 v32, v22, v32
	v_max_f32_e32 v224, v38, v24
	v_min_f32_e32 v24, v38, v24
	v_max_f32_e32 v47, v252, v251
	v_min_f32_e32 v251, v252, v251
	v_max_f32_e32 v48, v195, v190
	v_min_f32_e32 v190, v195, v190
	v_max_f32_e32 v51, v221, v23
	v_min_f32_e32 v23, v221, v23
	v_max_f32_e32 v27, v34, v240
	v_min_f32_e32 v240, v34, v240
	v_max_f32_e32 v53, v42, v224
	v_min_f32_e32 v224, v42, v224
	v_max_f32_e32 v31, v222, v24
	v_min_f32_e32 v24, v222, v24
	v_max_f32_e32 v29, v237, v21
	v_min_f32_e32 v21, v237, v21
	v_max_f32_e32 v59, v30, v32
	v_min_f32_e32 v32, v30, v32
	v_max_f32_e32 v41, v47, v48
	v_min_f32_e32 v48, v47, v48
	v_max_f32_e32 v62, v251, v190
	v_min_f32_e32 v190, v251, v190
	v_max_f32_e32 v19, v27, v23
	v_min_f32_e32 v23, v27, v23
	v_max_f32_e32 v37, v240, v41
	v_min_f32_e32 v41, v240, v41
	v_max_f32_e32 v56, v53, v29
	v_min_f32_e32 v29, v53, v29
	v_max_f32_e32 v173, v31, v21
	v_min_f32_e32 v21, v31, v21
	v_max_f32_e32 v63, v59, v224
	v_min_f32_e32 v224, v59, v224
	v_max_f32_e32 v212, v32, v24
	v_min_f32_e32 v24, v32, v24
	v_max_f32_e32 v33, v62, v48
	v_min_f32_e32 v48, v62, v48
	v_max_f32_e32 v57, v19, v56
	v_min_f32_e32 v56, v19, v56
	v_max_f32_e32 v26, v23, v29
	v_min_f32_e32 v29, v23, v29
	v_max_f32_e32 v225, v173, v63
	v_min_f32_e32 v63, v173, v63
	v_max_f32_e32 v210, v21, v224
	v_min_f32_e32 v224, v21, v224
	v_max_f32_e32 v227, v212, v33
	v_min_f32_e32 v33, v212, v33
	v_max_f32_e32 v52, v24, v48
	v_min_f32_e32 v48, v24, v48
	v_max_f32_e32 v226, v26, v56
	v_min_f32_e32 v56, v26, v56
	v_max_f32_e32 v228, v37, v29
	v_min_f32_e32 v29, v37, v29
	v_max_f32_e32 v60, v227, v41
	v_min_f32_e32 v41, v227, v41
	v_max_f32_e32 v183, v52, v33
	v_min_f32_e32 v33, v52, v33
	v_max_f32_e32 v182, v228, v225
	v_min_f32_e32 v225, v228, v225
	v_max_f32_e32 v242, v29, v63
	v_min_f32_e32 v63, v29, v63
	v_max_f32_e32 v241, v210, v60
	v_min_f32_e32 v60, v210, v60
	v_max_f32_e32 v244, v224, v41
	v_min_f32_e32 v41, v224, v41
	v_max_f32_e32 v243, v182, v56
	v_min_f32_e32 v56, v182, v56
	v_max_f32_e32 v245, v225, v242
	v_min_f32_e32 v242, v225, v242
	v_max_f32_e32 v247, v241, v63
	v_min_f32_e32 v63, v241, v63
	v_max_f32_e32 v232, v60, v244
	v_min_f32_e32 v244, v60, v244
	v_max_f32_e32 v234, v183, v41
	v_min_f32_e32 v41, v183, v41
	v_max_f32_e32 v236, v242, v247
	v_min_f32_e32 v247, v242, v247
	v_max_f32_e32 v235, v63, v232
	v_min_f32_e32 v232, v63, v232
	v_max_f32_e32 v246, v1, v12
	v_min_f32_e32 v12, v1, v12
	v_max_f32_e32 v248, v0, v16
	v_min_f32_e32 v16, v0, v16
	v_max_f32_e32 v250, v3, v25
	v_min_f32_e32 v25, v3, v25
	v_max_f32_e32 v249, v2, v28
	v_min_f32_e32 v28, v2, v28
	v_max_f32_e32 v18, v5, v9
	v_min_f32_e32 v9, v5, v9
	v_max_f32_e32 v238, v4, v7
	v_min_f32_e32 v7, v4, v7
	v_max_f32_e32 v20, v6, v10
	v_min_f32_e32 v10, v6, v10
	v_max_f32_e32 v35, v8, v11
	v_min_f32_e32 v11, v8, v11
	v_max_f32_e32 v22, v246, v238
	v_min_f32_e32 v238, v246, v238
	v_max_f32_e32 v38, v248, v20
	v_min_f32_e32 v20, v248, v20
	v_max_f32_e32 v252, v250, v35
	v_min_f32_e32 v35, v250, v35
	v_max_f32_e32 v195, v249, v18
	v_min_f32_e32 v18, v249, v18
	v_max_f32_e32 v221, v7, v12
	v_min_f32_e32 v12, v7, v12
	v_max_f32_e32 v34, v9, v28
	v_min_f32_e32 v28, v9, v28
	v_max_f32_e32 v42, v11, v25
	v_min_f32_e32 v25, v11, v25
	v_max_f32_e32 v222, v10, v16
	v_min_f32_e32 v16, v10, v16
	v_max_f32_e32 v237, v22, v38
	v_min_f32_e32 v38, v22, v38
	v_max_f32_e32 v30, v252, v195
	v_min_f32_e32 v195, v252, v195
	v_max_f32_e32 v47, v18, v238
	v_min_f32_e32 v238, v18, v238
	v_max_f32_e32 v251, v221, v34
	v_min_f32_e32 v34, v221, v34
	v_max_f32_e32 v27, v20, v35
	v_min_f32_e32 v35, v20, v35
	v_max_f32_e32 v240, v42, v222
	v_min_f32_e32 v222, v42, v222
	v_max_f32_e32 v53, v16, v12
	v_min_f32_e32 v12, v16, v12
	v_max_f32_e32 v31, v28, v25
	v_min_f32_e32 v25, v28, v25
	v_max_f32_e32 v59, v237, v30
	v_min_f32_e32 v30, v237, v30
	v_max_f32_e32 v32, v38, v195
	v_min_f32_e32 v195, v38, v195
	v_max_f32_e32 v62, v47, v240
	v_min_f32_e32 v240, v47, v240
	v_max_f32_e32 v19, v238, v222
	v_min_f32_e32 v222, v238, v222
	v_max_f32_e32 v23, v251, v27
	v_min_f32_e32 v27, v251, v27
	v_max_f32_e32 v173, v34, v35
	v_min_f32_e32 v35, v34, v35
	v_max_f32_e32 v21, v53, v31
	v_min_f32_e32 v31, v53, v31
	v_max_f32_e32 v212, v12, v25
	v_min_f32_e32 v25, v12, v25
	v_max_f32_e32 v24, v32, v30
	v_min_f32_e32 v30, v32, v30
	v_max_f32_e32 v26, v195, v21
	v_min_f32_e32 v21, v195, v21
	v_max_f32_e32 v37, v62, v23
	v_min_f32_e32 v23, v62, v23
	v_max_f32_e32 v227, v19, v27
	v_min_f32_e32 v27, v19, v27
	v_max_f32_e32 v52, v173, v240
	v_min_f32_e32 v240, v173, v240
	v_max_f32_e32 v228, v35, v222
	v_min_f32_e32 v222, v35, v222
	v_max_f32_e32 v29, v212, v31
	v_min_f32_e32 v31, v212, v31
	v_max_f32_e32 v210, v24, v37
	v_min_f32_e32 v37, v24, v37
	v_max_f32_e32 v224, v30, v23
	v_min_f32_e32 v23, v30, v23
	v_max_f32_e32 v182, v227, v52
	v_min_f32_e32 v52, v227, v52
	v_max_f32_e32 v225, v27, v240
	v_min_f32_e32 v240, v27, v240
	v_max_f32_e32 v241, v228, v29
	v_min_f32_e32 v29, v228, v29
	v_max_f32_e32 v60, v222, v31
	v_min_f32_e32 v31, v222, v31
	v_max_f32_e32 v183, v224, v37
	v_min_f32_e32 v37, v224, v37
	v_max_f32_e32 v242, v26, v23
	v_min_f32_e32 v23, v26, v23
	v_max_f32_e32 v63, v241, v21
	v_min_f32_e32 v21, v241, v21
	v_max_f32_e32 v1, v60, v29
	v_min_f32_e32 v29, v60, v29
	v_max_f32_e32 v0, v242, v182
	v_min_f32_e32 v182, v242, v182
	v_max_f32_e32 v3, v23, v52
	v_min_f32_e32 v52, v23, v52
	v_max_f32_e32 v2, v225, v63
	v_min_f32_e32 v63, v225, v63
	v_max_f32_e32 v5, v240, v21
	v_min_f32_e32 v21, v240, v21
	v_max_f32_e32 v4, v0, v37
	v_min_f32_e32 v37, v0, v37
	v_max_f32_e32 v6, v182, v3
	v_min_f32_e32 v3, v182, v3
	v_max_f32_e32 v8, v2, v52
	v_min_f32_e32 v52, v2, v52
	v_max_f32_e32 v246, v63, v5
	v_min_f32_e32 v5, v63, v5
	v_max_f32_e32 v248, v1, v21
	v_min_f32_e32 v21, v1, v21
	v_max_f32_e32 v250, v3, v8
	v_min_f32_e32 v8, v3, v8
	v_max_f32_e32 v249, v52, v246
	v_min_f32_e32 v246, v52, v246
	v_max_f32_e32 v40, v40, v239
	v_max_f32_e32 v55, v55, v43
	v_max_f32_e32 v61, v61, v44
	v_max_f32_e32 v213, v213, v36
	v_max_f32_e32 v50, v50, v218
	v_max_f32_e32 v215, v215, v230
	v_max_f32_e32 v15, v15, v216
	v_max_f32_e32 v217, v217, v219
	v_max_f32_e32 v17, v17, v233
	v_max_f32_e32 v13, v13, v220
	v_max_f32_e32 v214, v214, v231
	v_max_f32_e32 v14, v14, v49
	v_max_f32_e32 v46, v46, v229
	v_max_f32_e32 v54, v54, v211
	v_max_f32_e32 v39, v39, v58
	v_max_f32_e32 v223, v223, v45
	v_max_f32_e32 v7, v40, v17
	v_min_f32_e32 v17, v40, v17
	v_max_f32_e32 v9, v55, v13
	v_min_f32_e32 v13, v55, v13
	v_max_f32_e32 v11, v61, v214
	v_min_f32_e32 v214, v61, v214
	v_max_f32_e32 v10, v213, v14
	v_min_f32_e32 v14, v213, v14
	v_max_f32_e32 v22, v50, v46
	v_min_f32_e32 v46, v50, v46
	v_max_f32_e32 v252, v215, v54
	v_min_f32_e32 v54, v215, v54
	v_max_f32_e32 v18, v15, v39
	v_min_f32_e32 v39, v15, v39
	v_max_f32_e32 v221, v217, v223
	v_min_f32_e32 v223, v217, v223
	v_max_f32_e32 v20, v7, v22
	v_min_f32_e32 v22, v7, v22
	v_max_f32_e32 v42, v9, v252
	v_min_f32_e32 v252, v9, v252
	v_max_f32_e32 v16, v11, v18
	v_min_f32_e32 v18, v11, v18
	v_max_f32_e32 v28, v10, v221
	v_min_f32_e32 v221, v10, v221
	v_max_f32_e32 v237, v17, v46
	v_min_f32_e32 v46, v17, v46
	v_max_f32_e32 v38, v13, v54
	v_min_f32_e32 v54, v13, v54
	v_max_f32_e32 v47, v214, v39
	v_min_f32_e32 v39, v214, v39
	v_max_f32_e32 v238, v14, v223
	v_min_f32_e32 v223, v14, v223
	v_max_f32_e32 v251, v20, v16
	v_min_f32_e32 v16, v20, v16
	v_max_f32_e32 v34, v42, v28
	v_min_f32_e32 v28, v42, v28
	v_max_f32_e32 v53, v22, v18
	v_min_f32_e32 v18, v22, v18
	v_max_f32_e32 v12, v252, v221
	v_min_f32_e32 v221, v252, v221
	v_max_f32_e32 v32, v237, v47
	v_min_f32_e32 v47, v237, v47
	v_max_f32_e32 v195, v38, v238
	v_min_f32_e32 v238, v38, v238
	v_max_f32_e32 v62, v46, v39
	v_min_f32_e32 v39, v46, v39
	v_max_f32_e32 v19, v54, v223
	v_min_f32_e32 v223, v54, v223
	v_max_f32_e32 v173, v251, v34
	v_min_f32_e32 v34, v251, v34
	v_max_f32_e32 v35, v16, v28
	v_min_f32_e32 v28, v16, v28
	v_max_f32_e32 v212, v53, v12
	v_min_f32_e32 v12, v53, v12
	v_max_f32_e32 v24, v18, v221
	v_min_f32_e32 v221, v18, v221
	v_max_f32_e32 v30, v32, v195
	v_min_f32_e32 v195, v32, v195
	v_max_f32_e32 v227, v47, v238
	v_min_f32_e32 v238, v47, v238
	v_max_f32_e32 v27, v62, v19
	v_min_f32_e32 v19, v62, v19
	v_max_f32_e32 v228, v39, v223
	v_min_f32_e32 v223, v39, v223
	v_max_f32_e32 v51, v51, v25
	v_max_f32_e32 v57, v57, v31
	v_max_f32_e32 v226, v226, v29
	v_max_f32_e32 v243, v243, v21
	v_max_f32_e32 v56, v56, v248
	v_max_f32_e32 v245, v245, v5
	v_max_f32_e32 v236, v236, v246
	v_max_f32_e32 v247, v247, v249
	v_max_f32_e32 v235, v235, v8
	v_max_f32_e32 v232, v232, v250
	v_max_f32_e32 v244, v244, v6
	v_max_f32_e32 v234, v234, v37
	v_max_f32_e32 v41, v41, v4
	v_max_f32_e32 v33, v33, v183
	v_max_f32_e32 v48, v48, v210
	v_max_f32_e32 v190, v190, v59
	v_max_f32_e32 v222, v51, v235
	v_min_f32_e32 v235, v51, v235
	v_max_f32_e32 v224, v57, v232
	v_min_f32_e32 v232, v57, v232
	v_max_f32_e32 v26, v226, v244
	v_min_f32_e32 v244, v226, v244
	v_max_f32_e32 v241, v243, v234
	v_min_f32_e32 v234, v243, v234
	v_max_f32_e32 v60, v56, v41
	v_min_f32_e32 v41, v56, v41
	v_max_f32_e32 v242, v245, v33
	v_min_f32_e32 v33, v245, v33
	v_max_f32_e32 v23, v236, v48
	v_min_f32_e32 v48, v236, v48
	v_max_f32_e32 v225, v247, v190
	v_min_f32_e32 v190, v247, v190
	v_max_f32_e32 v240, v222, v60
	v_min_f32_e32 v60, v222, v60
	v_max_f32_e32 v0, v224, v242
	v_min_f32_e32 v242, v224, v242
	v_max_f32_e32 v182, v26, v23
	v_min_f32_e32 v23, v26, v23
	v_max_f32_e32 v2, v241, v225
	v_min_f32_e32 v225, v241, v225
	v_max_f32_e32 v63, v235, v41
	v_min_f32_e32 v41, v235, v41
	v_max_f32_e32 v1, v232, v33
	v_min_f32_e32 v33, v232, v33
	v_max_f32_e32 v3, v244, v48
	v_min_f32_e32 v48, v244, v48
	v_max_f32_e32 v52, v234, v190
	v_min_f32_e32 v190, v234, v190
	v_max_f32_e32 v239, v240, v182
	v_min_f32_e32 v182, v240, v182
	v_max_f32_e32 v43, v0, v2
	v_min_f32_e32 v2, v0, v2
	v_max_f32_e32 v44, v60, v23
	v_min_f32_e32 v23, v60, v23
	v_max_f32_e32 v36, v242, v225
	v_min_f32_e32 v225, v242, v225
	v_max_f32_e32 v218, v63, v3
	v_min_f32_e32 v3, v63, v3
	v_max_f32_e32 v230, v1, v52
	v_min_f32_e32 v52, v1, v52
	v_max_f32_e32 v216, v41, v48
	v_min_f32_e32 v48, v41, v48
	v_max_f32_e32 v219, v33, v190
	v_min_f32_e32 v190, v33, v190
	v_max_f32_e32 v233, v239, v43
	v_min_f32_e32 v43, v239, v43
	v_max_f32_e32 v220, v182, v2
	v_min_f32_e32 v2, v182, v2
	v_max_f32_e32 v231, v44, v36
	v_min_f32_e32 v36, v44, v36
	v_max_f32_e32 v49, v23, v225
	v_min_f32_e32 v225, v23, v225
	v_max_f32_e32 v229, v218, v230
	v_min_f32_e32 v230, v218, v230
	v_max_f32_e32 v211, v3, v52
	v_min_f32_e32 v52, v3, v52
	v_max_f32_e32 v58, v216, v219
	v_min_f32_e32 v219, v216, v219
	v_max_f32_e32 v45, v48, v190
	v_min_f32_e32 v190, v48, v190
	v_max_f32_e32 v173, v173, v190
	v_max_f32_e32 v34, v34, v45
	v_max_f32_e32 v35, v35, v219
	v_max_f32_e32 v28, v28, v58
	v_max_f32_e32 v212, v212, v52
	v_max_f32_e32 v12, v12, v211
	v_max_f32_e32 v24, v24, v230
	v_max_f32_e32 v221, v221, v229
	v_max_f32_e32 v30, v30, v225
	v_max_f32_e32 v195, v195, v49
	v_max_f32_e32 v227, v227, v36
	v_max_f32_e32 v238, v238, v231
	v_max_f32_e32 v27, v27, v2
	v_max_f32_e32 v19, v19, v220
	v_max_f32_e32 v228, v228, v43
	v_max_f32_e32 v223, v223, v233
	v_max_f32_e32 v40, v173, v30
	v_min_f32_e32 v30, v173, v30
	v_max_f32_e32 v55, v34, v195
	v_min_f32_e32 v195, v34, v195
	v_max_f32_e32 v61, v35, v227
	v_min_f32_e32 v227, v35, v227
	v_max_f32_e32 v213, v28, v238
	v_min_f32_e32 v238, v28, v238
	v_max_f32_e32 v50, v212, v27
	v_min_f32_e32 v27, v212, v27
	v_max_f32_e32 v215, v12, v19
	v_min_f32_e32 v19, v12, v19
	v_max_f32_e32 v15, v24, v228
	v_min_f32_e32 v228, v24, v228
	v_max_f32_e32 v217, v221, v223
	v_min_f32_e32 v223, v221, v223
	v_max_f32_e32 v7, v40, v50
	v_min_f32_e32 v50, v40, v50
	v_max_f32_e32 v9, v55, v215
	v_min_f32_e32 v215, v55, v215
	v_max_f32_e32 v11, v61, v15
	v_min_f32_e32 v15, v61, v15
	v_max_f32_e32 v10, v213, v217
	v_min_f32_e32 v217, v213, v217
	v_max_f32_e32 v17, v30, v27
	v_min_f32_e32 v27, v30, v27
	v_max_f32_e32 v13, v195, v19
	v_min_f32_e32 v19, v195, v19
	v_max_f32_e32 v214, v227, v228
	v_min_f32_e32 v228, v227, v228
	v_max_f32_e32 v14, v238, v223
	v_min_f32_e32 v223, v238, v223
	v_max_f32_e32 v20, v7, v11
	v_min_f32_e32 v11, v7, v11
	v_max_f32_e32 v42, v9, v10
	v_min_f32_e32 v10, v9, v10
	v_max_f32_e32 v22, v50, v15
	v_min_f32_e32 v15, v50, v15
	v_max_f32_e32 v252, v215, v217
	v_min_f32_e32 v217, v215, v217
	v_max_f32_e32 v237, v17, v214
	v_min_f32_e32 v214, v17, v214
	v_max_f32_e32 v38, v13, v14
	v_min_f32_e32 v14, v13, v14
	v_max_f32_e32 v46, v27, v228
	v_min_f32_e32 v228, v27, v228
	v_max_f32_e32 v54, v19, v223
	v_min_f32_e32 v223, v19, v223
	v_max_f32_e32 v251, v20, v42
	v_min_f32_e32 v42, v20, v42
	v_max_f32_e32 v16, v11, v10
	v_min_f32_e32 v10, v11, v10
	v_max_f32_e32 v53, v22, v252
	v_min_f32_e32 v252, v22, v252
	v_max_f32_e32 v18, v15, v217
	v_min_f32_e32 v217, v15, v217
	v_max_f32_e32 v32, v237, v38
	v_min_f32_e32 v38, v237, v38
	v_max_f32_e32 v47, v214, v14
	v_min_f32_e32 v14, v214, v14
	v_max_f32_e32 v62, v46, v54
	v_min_f32_e32 v54, v46, v54
	v_max_f32_e32 v39, v228, v223
	v_min_f32_e32 v223, v228, v223
	v_mov_b32_e32 v2, v251
	v_mov_b32_e32 v9, v42
	v_mov_b32_e32 v11, v16
	v_mov_b32_e32 v6, v10
	v_mov_b32_e32 v15, v53
	v_mov_b32_e32 v16, v18
	v_mov_b32_e32 v5, v217
	v_mov_b32_e32 v12, v32
	v_mov_b32_e32 v10, v38
	v_mov_b32_e32 v13, v47
	v_mov_b32_e32 v4, v14
	v_mov_b32_e32 v8, v62
	v_mov_b32_e32 v3, v54
	v_mov_b32_e32 v7, v39
	v_mov_b32_e32 v0, v223
	v_mov_b32_e32 v14, v252
	v_mov_b32_e32 v27, v0
	s_nop 1
	v_permlane32_swap_b32 v27, v27
	v_mov_b32_e32 v29, v7
	s_nop 1
	v_permlane32_swap_b32 v29, v29
	v_mov_b32_e32 v31, v3
	s_nop 1
	v_permlane32_swap_b32 v31, v31
	v_mov_b32_e32 v30, v8
	s_nop 1
	v_permlane32_swap_b32 v30, v30
	v_mov_b32_e32 v28, v4
	s_nop 1
	v_permlane32_swap_b32 v28, v28
	v_mov_b32_e32 v26, v13
	s_nop 1
	v_permlane32_swap_b32 v26, v26
	s_waitcnt lgkmcnt(5)
	v_mov_b32_e32 v1, v2
	s_nop 1
	v_permlane32_swap_b32 v1, v1
	v_mov_b32_e32 v25, v10
	s_nop 1
	v_permlane32_swap_b32 v25, v25
	v_max_f32_e32 v2, v2, v27
	s_waitcnt lgkmcnt(6)
	v_mov_b32_e32 v17, v9
	s_nop 1
	v_permlane32_swap_b32 v17, v17
	v_mov_b32_e32 v24, v12
	s_nop 1
	v_permlane32_swap_b32 v24, v24
	v_max_f32_e32 v9, v9, v29
	s_waitcnt lgkmcnt(7)
	v_mov_b32_e32 v18, v11
	s_nop 1
	v_permlane32_swap_b32 v18, v18
	v_mov_b32_e32 v23, v5
	s_nop 1
	v_permlane32_swap_b32 v23, v23
	v_max_f32_e32 v11, v11, v31
	s_waitcnt lgkmcnt(8)
	v_mov_b32_e32 v19, v6
	s_nop 1
	v_permlane32_swap_b32 v19, v19
	v_mov_b32_e32 v22, v16
	s_nop 1
	v_permlane32_swap_b32 v22, v22
	v_max_f32_e32 v6, v6, v30
	s_waitcnt lgkmcnt(9)
	v_mov_b32_e32 v20, v15
	s_nop 1
	v_permlane32_swap_b32 v20, v20
	v_mov_b32_e32 v21, v14
	s_nop 1
	v_permlane32_swap_b32 v21, v21
	v_max_f32_e32 v15, v15, v28
	s_waitcnt lgkmcnt(10)
	v_max_f32_e32 v14, v14, v26
	s_waitcnt lgkmcnt(8)
	v_max_f32_e32 v16, v16, v25
	s_waitcnt lgkmcnt(6)
	v_max_f32_e32 v5, v5, v24
	s_waitcnt lgkmcnt(4)
	v_max_f32_e32 v12, v12, v23
	s_waitcnt lgkmcnt(2)
	v_max_f32_e32 v10, v10, v22
	s_waitcnt lgkmcnt(0)
	v_max_f32_e32 v13, v13, v21
	v_max_f32_e32 v4, v4, v20
	v_max_f32_e32 v8, v8, v19
	v_max_f32_e32 v3, v3, v18
	v_max_f32_e32 v7, v7, v17
	v_max_f32_e32 v0, v0, v1
	v_max_f32_e32 v1, v2, v12
	v_min_f32_e32 v2, v2, v12
	v_max_f32_e32 v12, v9, v10
	v_min_f32_e32 v9, v9, v10
	v_max_f32_e32 v10, v11, v13
	v_min_f32_e32 v11, v11, v13
	v_max_f32_e32 v13, v6, v4
	v_min_f32_e32 v4, v6, v4
	v_max_f32_e32 v6, v15, v8
	v_min_f32_e32 v8, v15, v8
	v_max_f32_e32 v15, v14, v3
	v_min_f32_e32 v3, v14, v3
	v_max_f32_e32 v14, v16, v7
	v_min_f32_e32 v7, v16, v7
	v_max_f32_e32 v16, v5, v0
	v_min_f32_e32 v0, v5, v0
	v_max_f32_e32 v5, v1, v6
	v_min_f32_e32 v1, v1, v6
	v_max_f32_e32 v6, v12, v15
	v_min_f32_e32 v12, v12, v15
	v_max_f32_e32 v15, v10, v14
	v_min_f32_e32 v10, v10, v14
	v_max_f32_e32 v14, v13, v16
	v_min_f32_e32 v13, v13, v16
	v_max_f32_e32 v16, v2, v8
	v_min_f32_e32 v2, v2, v8
	v_max_f32_e32 v8, v9, v3
	v_min_f32_e32 v3, v9, v3
	v_max_f32_e32 v9, v11, v7
	v_min_f32_e32 v7, v11, v7
	v_max_f32_e32 v11, v4, v0
	v_min_f32_e32 v0, v4, v0
	v_max_f32_e32 v4, v5, v15
	v_min_f32_e32 v5, v5, v15
	v_max_f32_e32 v15, v6, v14
	v_min_f32_e32 v6, v6, v14
	v_max_f32_e32 v14, v1, v10
	v_min_f32_e32 v1, v1, v10
	v_max_f32_e32 v10, v12, v13
	v_min_f32_e32 v12, v12, v13
	v_max_f32_e32 v13, v16, v9
	v_min_f32_e32 v9, v16, v9
	v_max_f32_e32 v16, v8, v11
	v_min_f32_e32 v8, v8, v11
	v_max_f32_e32 v11, v2, v7
	v_min_f32_e32 v2, v2, v7
	v_max_f32_e32 v7, v3, v0
	v_min_f32_e32 v0, v3, v0
	v_max_f32_e32 v3, v4, v15
	v_min_f32_e32 v4, v4, v15
	v_max_f32_e32 v15, v5, v6
	v_min_f32_e32 v5, v5, v6
	v_max_f32_e32 v6, v14, v10
	v_min_f32_e32 v10, v14, v10
	v_max_f32_e32 v14, v1, v12
	v_min_f32_e32 v1, v1, v12
	v_max_f32_e32 v12, v13, v16
	v_min_f32_e32 v13, v13, v16
	v_max_f32_e32 v16, v9, v8
	v_min_f32_e32 v8, v9, v8
	v_max_f32_e32 v9, v11, v7
	v_min_f32_e32 v7, v11, v7
	v_max_f32_e32 v11, v2, v0
	v_min_f32_e32 v0, v2, v0
	v_lshl_add_u32 v2, s8, 12, v207
	ds_write2st64_b32 v2, v3, v4 offset1:1
	ds_write2st64_b32 v2, v15, v5 offset0:2 offset1:3
	ds_write2st64_b32 v2, v6, v10 offset0:4 offset1:5
	ds_write2st64_b32 v2, v14, v1 offset0:6 offset1:7
	ds_write2st64_b32 v2, v12, v13 offset0:8 offset1:9
	ds_write2st64_b32 v2, v16, v8 offset0:10 offset1:11
	ds_write2st64_b32 v2, v9, v7 offset0:12 offset1:13
	ds_write2st64_b32 v2, v11, v0 offset0:14 offset1:15
	s_mov_b64 s[6:7], 0
	s_mov_b32 s8, 1
	s_cbranch_vccz .LBB0_704
	ds_read2st64_b32 v[0:1], v207 offset1:1
	ds_read2st64_b32 v[2:3], v207 offset0:2 offset1:3
	ds_read2st64_b32 v[4:5], v207 offset0:4 offset1:5
	ds_read2st64_b32 v[6:7], v207 offset0:6 offset1:7
	ds_read2st64_b32 v[16:17], v207 offset0:16 offset1:17
	ds_read2st64_b32 v[18:19], v207 offset0:18 offset1:19
	ds_read2st64_b32 v[20:21], v207 offset0:20 offset1:21
	ds_read2st64_b32 v[22:23], v207 offset0:22 offset1:23
	ds_read2st64_b32 v[8:9], v207 offset0:8 offset1:9
	ds_read2st64_b32 v[10:11], v207 offset0:10 offset1:11
	ds_read2st64_b32 v[12:13], v207 offset0:12 offset1:13
	ds_read2st64_b32 v[14:15], v207 offset0:14 offset1:15
	ds_read2st64_b32 v[24:25], v207 offset0:24 offset1:25
	ds_read2st64_b32 v[26:27], v207 offset0:26 offset1:27
	ds_read2st64_b32 v[28:29], v207 offset0:28 offset1:29
	ds_read2st64_b32 v[30:31], v207 offset0:30 offset1:31
	s_and_saveexec_b64 s[8:9], s[38:39]
	s_cbranch_execz .LBB0_696
	s_waitcnt lgkmcnt(0)
	v_and_b32_e32 v49, 0xffffff80, v30
	v_and_b32_e32 v48, 0xffffff80, v0
	v_and_b32_e32 v39, 0xffffff80, v19
	v_and_b32_e32 v38, 0xffffff80, v20
	v_pk_add_f32 v[52:53], v[38:39], v[48:49] op_sel:[1,0] op_sel_hi:[0,1]
	v_cmp_gt_i32_e32 vcc, 0, v52
	v_bfrev_b32_e32 v43, 0.5
	s_movk_i32 s12, 0xff00
	v_cndmask_b32_e64 v43, v43, 3, vcc
	v_and_b32_e32 v42, 0xffffff80, v23
	v_and_or_b32 v56, v52, s12, v43
	v_mov_b32_e32 v43, v38
	v_pk_add_f32 v[52:53], v[48:49], v[42:43] op_sel_hi:[0,1]
	v_cmp_gt_i32_e32 vcc, 0, v53
	v_mov_b32_e32 v54, 0xfb
	v_and_b32_e32 v41, 0xffffff80, v22
	v_cndmask_b32_e64 v54, v54, 4, vcc
	v_and_b32_e32 v40, 0xffffff80, v21
	v_and_or_b32 v53, v53, s12, v54
	v_cmp_gt_i32_e32 vcc, 0, v52
	v_mov_b32_e32 v54, 0xf8
	v_mov_b32_e32 v58, 0xf9
	v_cndmask_b32_e64 v57, v54, 7, vcc
	v_pk_add_f32 v[54:55], v[48:49], v[40:41] op_sel_hi:[0,1]
	v_cmp_gt_i32_e32 vcc, 0, v55
	v_mov_b32_e32 v59, 0xfa
	v_and_b32_e32 v55, 0xffffff00, v55
	v_cndmask_b32_e64 v58, v58, 6, vcc
	v_cmp_gt_i32_e32 vcc, 0, v54
	v_and_b32_e32 v54, 0xffffff00, v54
	v_and_b32_e32 v52, 0xffffff00, v52
	v_cndmask_b32_e64 v59, v59, 5, vcc
	v_or_b32_e32 v55, v58, v55
	v_or_b32_e32 v54, v59, v54
	v_or_b32_e32 v52, v57, v52
	v_writelane_b32 v255, s8, 44
	v_min_f32_e32 v57, v55, v52
	v_max_f32_e32 v58, v53, v54
	v_min_f32_e32 v53, v53, v54
	v_max_f32_e32 v52, v55, v52
	v_writelane_b32 v255, s9, 45
	v_and_b32_e32 v45, 0xffffff80, v24
	v_and_b32_e32 v44, 0xffffff80, v27
	v_min_f32_e32 v59, v58, v57
	v_min_f32_e32 v54, v53, v52
	v_max_f32_e32 v57, v58, v57
	v_max_f32_e32 v52, v53, v52
	v_pk_add_f32 v[44:45], v[48:49], v[44:45] op_sel_hi:[0,1]
	v_and_b32_e32 v47, 0xffffff80, v26
	v_min_f32_e32 v58, v57, v52
	v_max_f32_e32 v57, v57, v52
	v_cmp_gt_i32_e32 vcc, 0, v45
	v_mov_b32_e32 v52, 0xf7
	v_and_b32_e32 v46, 0xffffff80, v25
	v_cndmask_b32_e64 v52, v52, 8, vcc
	v_and_or_b32 v45, v45, s12, v52
	v_cmp_gt_i32_e32 vcc, 0, v44
	v_mov_b32_e32 v52, 0xf4
	v_pk_add_f32 v[46:47], v[48:49], v[46:47] op_sel_hi:[0,1]
	v_cndmask_b32_e64 v52, v52, 11, vcc
	v_cmp_gt_i32_e32 vcc, 0, v47
	v_mov_b32_e32 v53, 0xf5
	v_min_f32_e32 v55, v59, v54
	v_max_f32_e32 v59, v59, v54
	v_cndmask_b32_e64 v53, v53, 10, vcc
	v_cmp_gt_i32_e32 vcc, 0, v46
	v_mov_b32_e32 v54, 0xf6
	v_and_b32_e32 v47, 0xffffff00, v47
	v_cndmask_b32_e64 v54, v54, 9, vcc
	v_and_b32_e32 v46, 0xffffff00, v46
	v_and_b32_e32 v44, 0xffffff00, v44
	v_or_b32_e32 v47, v53, v47
	v_or_b32_e32 v46, v54, v46
	v_or_b32_e32 v44, v52, v44
	v_and_b32_e32 v51, 0xffffff80, v29
	v_and_b32_e32 v50, 0xffffff80, v28
	v_writelane_b32 v255, s11, 46
	v_min_f32_e32 v52, v47, v44
	v_max_f32_e32 v53, v45, v46
	v_min_f32_e32 v46, v45, v46
	v_max_f32_e32 v47, v47, v44
	v_pk_add_f32 v[44:45], v[48:49], v[50:51] op_sel_hi:[0,1]
	v_cmp_gt_i32_e64 s[10:11], 0, v45
	v_mov_b32_e32 v50, 0xf2
	v_mov_b32_e32 v51, 0xf3
	v_cndmask_b32_e64 v50, v50, 13, s[10:11]
	v_cmp_gt_i32_e64 s[10:11], 0, v44
	v_and_b32_e32 v45, 0xffffff00, v45
	v_and_b32_e32 v44, 0xffffff00, v44
	v_cndmask_b32_e64 v51, v51, 12, s[10:11]
	v_or_b32_e32 v50, v50, v45
	v_or_b32_e32 v51, v51, v44
	v_and_b32_e32 v45, 0xffffff80, v31
	v_mov_b32_e32 v44, v49
	v_pk_add_f32 v[44:45], v[48:49], v[44:45] op_sel_hi:[0,1]
	v_cmp_gt_i32_e64 s[42:43], 0, v45
	v_mov_b32_e32 v249, 0xf0
	v_mov_b32_e32 v173, 0xf1
	v_cndmask_b32_e64 v63, v249, 15, s[42:43]
	v_cmp_gt_i32_e64 s[42:43], 0, v44
	v_and_b32_e32 v45, 0xffffff00, v45
	v_and_b32_e32 v44, 0xffffff00, v44
	v_cndmask_b32_e64 v173, v173, 14, s[42:43]
	v_or_b32_e32 v45, v63, v45
	v_or_b32_e32 v44, v173, v44
	v_max_f32_e32 v62, v51, v50
	v_min_f32_e32 v63, v44, v45
	v_min_f32_e32 v50, v51, v50
	v_max_f32_e32 v44, v44, v45
	v_max_f32_e32 v54, v53, v52
	v_max_f32_e32 v60, v46, v47
	v_min_f32_e32 v173, v62, v63
	v_min_f32_e32 v45, v50, v44
	v_min_f32_e32 v51, v53, v52
	v_min_f32_e32 v46, v46, v47
	v_max_f32_e32 v52, v62, v63
	v_max_f32_e32 v44, v50, v44
	v_max_f32_e32 v61, v54, v60
	v_min_f32_e32 v178, v173, v45
	v_max_f32_e32 v47, v51, v46
	v_min_f32_e32 v50, v52, v44
	v_min_f32_e32 v54, v54, v60
	v_max_f32_e32 v45, v173, v45
	v_min_f32_e32 v46, v51, v46
	v_max_f32_e32 v44, v52, v44
	v_min_f32_e32 v179, v61, v178
	v_min_f32_e32 v53, v47, v50
	v_min_f32_e32 v60, v54, v45
	v_min_f32_e32 v52, v46, v44
	v_max_f32_e32 v61, v61, v178
	v_max_f32_e32 v47, v47, v50
	v_max_f32_e32 v45, v54, v45
	v_max_f32_e32 v44, v46, v44
	v_min_f32_e32 v62, v179, v53
	v_min_f32_e32 v63, v60, v52
	v_min_f32_e32 v50, v61, v47
	v_min_f32_e32 v46, v45, v44
	v_max_f32_e32 v53, v179, v53
	v_max_f32_e32 v52, v60, v52
	v_max_f32_e32 v47, v61, v47
	v_max_f32_e32 v44, v45, v44
	v_min_f32_e32 v60, v53, v52
	v_min_f32_e32 v61, v47, v44
	v_max_f32_e32 v52, v53, v52
	v_max_f32_e32 v53, v47, v44
	v_and_b32_e32 v44, 0xffffff80, v1
	v_add_f32_e32 v45, v39, v44
	v_min_f32_e32 v51, v62, v63
	v_min_f32_e32 v173, v50, v46
	v_max_f32_e32 v62, v62, v63
	v_max_f32_e32 v63, v50, v46
	v_cmp_gt_i32_e32 vcc, 0, v45
	v_mov_b32_e32 v46, 0xec
	v_mov_b32_e32 v47, 0xe9
	v_cndmask_b32_e64 v46, v46, 19, vcc
	v_and_or_b32 v45, v45, s12, v46
	v_pk_add_f32 v[42:43], v[44:45], v[42:43] op_sel_hi:[0,1]
	v_cmp_gt_i32_e32 vcc, 0, v43
	v_mov_b32_e32 v46, 0xeb
	v_pk_add_f32 v[40:41], v[44:45], v[40:41] op_sel_hi:[0,1]
	v_cndmask_b32_e64 v46, v46, 20, vcc
	v_and_or_b32 v43, v43, s12, v46
	v_cmp_gt_i32_e32 vcc, 0, v42
	v_mov_b32_e32 v46, 0xe8
	v_mov_b32_e32 v50, 0xea
	v_cndmask_b32_e64 v46, v46, 23, vcc
	v_cmp_gt_i32_e32 vcc, 0, v41
	v_and_b32_e32 v41, 0xffffff00, v41
	v_and_b32_e32 v42, 0xffffff00, v42
	v_cndmask_b32_e64 v47, v47, 22, vcc
	v_cmp_gt_i32_e32 vcc, 0, v40
	v_and_b32_e32 v40, 0xffffff00, v40
	v_or_b32_e32 v41, v47, v41
	v_cndmask_b32_e64 v50, v50, 21, vcc
	v_or_b32_e32 v40, v50, v40
	v_or_b32_e32 v42, v46, v42
	v_and_b32_e32 v182, 0xffffff80, v3
	v_min_f32_e32 v46, v41, v42
	v_max_f32_e32 v47, v43, v40
	v_min_f32_e32 v40, v43, v40
	v_max_f32_e32 v41, v41, v42
	v_and_b32_e32 v37, 0xffffff80, v4
	v_max_f32_e32 v43, v47, v46
	v_min_f32_e32 v42, v40, v41
	v_max_f32_e32 v40, v40, v41
	v_min_f32_e32 v50, v47, v46
	v_and_b32_e32 v46, 0xffffff80, v2
	v_and_b32_e32 v36, 0xffffff80, v18
	v_min_f32_e32 v179, v43, v40
	v_max_f32_e32 v180, v43, v40
	v_pk_add_f32 v[40:41], v[46:47], v[38:39] op_sel_hi:[0,1]
	v_cmp_gt_i32_e32 vcc, 0, v41
	v_mov_b32_e32 v38, 0xdc
	v_and_b32_e32 v35, 0xffffff80, v7
	v_cndmask_b32_e64 v38, v38, 35, vcc
	v_and_or_b32 v41, v41, s12, v38
	v_cmp_gt_i32_e32 vcc, 0, v40
	v_mov_b32_e32 v38, 0xdb
	v_and_b32_e32 v34, 0xffffff80, v17
	v_cndmask_b32_e64 v38, v38, 36, vcc
	v_and_or_b32 v181, v40, s12, v38
	v_add_f32_e32 v38, v39, v182
	v_cmp_gt_i32_e32 vcc, 0, v38
	v_mov_b32_e32 v39, 0xcc
	s_nop 0
	v_cndmask_b32_e64 v39, v39, 51, vcc
	v_and_or_b32 v54, v38, s12, v39
	v_pk_add_f32 v[38:39], v[48:49], v[36:37]
	v_min_f32_e32 v178, v50, v42
	v_cmp_gt_i32_e32 vcc, 0, v38
	v_bfrev_b32_e32 v39, -0.5
	v_max_f32_e32 v50, v50, v42
	v_cndmask_b32_e64 v39, v39, 2, vcc
	v_and_or_b32 v38, v38, s12, v39
	v_mov_b32_e32 v39, 0xed
	v_and_b32_e32 v43, 0xffffff80, v6
	v_min_f32_e32 v183, v38, v56
	v_max_f32_e32 v56, v38, v56
	v_add_f32_e32 v38, v36, v44
	v_cmp_gt_i32_e32 vcc, 0, v38
	v_and_b32_e32 v42, 0xffffff80, v5
	v_and_b32_e32 v33, 0xffffff80, v14
	v_cndmask_b32_e64 v39, v39, 18, vcc
	v_and_or_b32 v38, v38, s12, v39
	v_mov_b32_e32 v39, 0xdd
	v_and_b32_e32 v32, 0xffffff80, v16
	v_min_f32_e32 v190, v38, v45
	v_max_f32_e32 v195, v38, v45
	v_add_f32_e32 v38, v36, v46
	v_cmp_gt_i32_e32 vcc, 0, v38
	v_mov_b32_e32 v45, 0x61
	v_mov_b32_e32 v234, 0xef
	v_cndmask_b32_e64 v39, v39, 34, vcc
	v_and_or_b32 v38, v38, s12, v39
	v_mov_b32_e32 v39, 0xcd
	v_mov_b32_e32 v241, 0xdf
	v_min_f32_e32 v209, v38, v41
	v_max_f32_e32 v210, v38, v41
	v_add_f32_e32 v38, v36, v182
	v_cmp_gt_i32_e32 vcc, 0, v38
	v_mov_b32_e32 v41, 0x42
	v_mov_b32_e32 v244, 0xcf
	v_cndmask_b32_e64 v39, v39, 50, vcc
	v_and_or_b32 v40, v38, s12, v39
	v_pk_add_f32 v[38:39], v[36:37], v[36:37] op_sel:[1,0] op_sel_hi:[0,1]
	v_cmp_gt_i32_e32 vcc, 0, v38
	v_mov_b32_e32 v39, 0xbd
	v_and_b32_e32 v47, 0xffffff80, v8
	v_cndmask_b32_e32 v39, v39, v41, vcc
	v_and_or_b32 v41, v38, s12, v39
	v_pk_add_f32 v[38:39], v[48:49], v[34:35]
	v_pk_add_f32 v[48:49], v[48:49], v[32:33]
	v_cmp_gt_i32_e32 vcc, 0, v38
	v_mov_b32_e32 v39, 0xfe
	s_mov_b32 s28, 0xff61b1e6
	v_cndmask_b32_e64 v39, v39, 1, vcc
	v_and_or_b32 v211, v38, s12, v39
	v_add_f32_e32 v38, v34, v44
	v_cmp_gt_i32_e32 vcc, 0, v38
	v_mov_b32_e32 v39, 0xee
	v_add_f32_e32 v44, v32, v44
	v_cndmask_b32_e64 v39, v39, 17, vcc
	v_and_or_b32 v212, v38, s12, v39
	v_add_f32_e32 v38, v34, v46
	v_cmp_gt_i32_e32 vcc, 0, v38
	v_mov_b32_e32 v39, 0xde
	v_add_f32_e32 v46, v32, v46
	v_cndmask_b32_e64 v39, v39, 33, vcc
	v_and_or_b32 v213, v38, s12, v39
	v_add_f32_e32 v38, v34, v182
	v_cmp_gt_i32_e32 vcc, 0, v38
	v_mov_b32_e32 v39, 0xce
	v_add_f32_e32 v182, v32, v182
	v_cndmask_b32_e64 v39, v39, 49, vcc
	v_and_or_b32 v38, v38, s12, v39
	v_cmp_gt_i32_e64 s[74:75], 0, v46
	v_cmp_gt_i32_e64 s[84:85], 0, v182
	v_min_f32_e32 v219, v38, v40
	v_max_f32_e32 v220, v38, v40
	v_pk_add_f32 v[38:39], v[36:37], v[34:35] op_sel:[1,0] op_sel_hi:[0,1]
	v_cmp_gt_i32_e32 vcc, 0, v38
	v_mov_b32_e32 v39, 0xbe
	v_mov_b32_e32 v40, 0x41
	v_cndmask_b32_e32 v39, v39, v40, vcc
	v_and_or_b32 v38, v38, s12, v39
	v_mov_b32_e32 v40, v35
	v_cndmask_b32_e64 v241, v241, 32, s[74:75]
	v_min_f32_e32 v215, v38, v41
	v_max_f32_e32 v216, v38, v41
	v_pk_add_f32 v[38:39], v[34:35], v[42:43]
	v_mov_b32_e32 v41, v43
	v_pk_add_f32 v[40:41], v[34:35], v[40:41] op_sel_hi:[0,1]
	v_cmp_gt_i32_e32 vcc, 0, v38
	v_mov_b32_e32 v34, 0xae
	v_mov_b32_e32 v39, 0x51
	v_cndmask_b32_e32 v34, v34, v39, vcc
	v_cmp_gt_i32_e32 vcc, 0, v41
	v_mov_b32_e32 v39, 0x9e
	v_and_b32_e32 v38, 0xffffff00, v38
	v_cndmask_b32_e32 v39, v39, v45, vcc
	v_or_b32_e32 v218, v34, v38
	v_cmp_gt_i32_e32 vcc, 0, v40
	v_mov_b32_e32 v34, 0x8e
	v_mov_b32_e32 v38, 0x71
	v_cndmask_b32_e32 v34, v34, v38, vcc
	v_and_or_b32 v214, v40, s12, v34
	v_cmp_gt_i32_e32 vcc, 0, v48
	v_mov_b32_e32 v34, 0xff
	v_cndmask_b32_e64 v244, v244, 48, s[84:85]
	v_cndmask_b32_e64 v34, v34, 0, vcc
	v_and_or_b32 v34, v48, s12, v34
	v_and_or_b32 v46, v46, s12, v241
	v_and_or_b32 v182, v182, s12, v244
	v_max_f32_e32 v48, v34, v211
	v_min_f32_e32 v34, v34, v211
	v_max_f32_e32 v49, v48, v183
	v_max_f32_e32 v211, v34, v56
	v_min_f32_e32 v48, v48, v183
	v_min_f32_e32 v34, v34, v56
	v_max_f32_e32 v221, v49, v211
	v_max_f32_e32 v56, v48, v34
	v_min_f32_e32 v49, v49, v211
	v_min_f32_e32 v34, v48, v34
	v_max_f32_e32 v222, v221, v55
	v_max_f32_e32 v183, v56, v58
	v_max_f32_e32 v211, v49, v59
	v_max_f32_e32 v48, v34, v57
	v_min_f32_e32 v55, v221, v55
	v_min_f32_e32 v56, v56, v58
	v_min_f32_e32 v49, v49, v59
	v_min_f32_e32 v34, v34, v57
	v_max_f32_e32 v241, v46, v213
	v_max_f32_e32 v58, v55, v56
	v_max_f32_e32 v57, v49, v34
	v_min_f32_e32 v55, v55, v56
	v_min_f32_e32 v34, v49, v34
	v_min_f32_e32 v46, v46, v213
	v_max_f32_e32 v244, v181, v182
	v_max_f32_e32 v49, v55, v34
	v_min_f32_e32 v34, v55, v34
	v_cmp_gt_i32_e64 s[6:7], 0, v44
	v_min_f32_e32 v181, v181, v182
	s_nop 0
	v_cndmask_b32_e64 v234, v234, 16, s[6:7]
	v_and_or_b32 v44, v44, s12, v234
	v_max_f32_e32 v234, v44, v212
	v_min_f32_e32 v44, v44, v212
	v_max_f32_e32 v235, v234, v190
	v_max_f32_e32 v212, v44, v195
	v_min_f32_e32 v190, v234, v190
	v_min_f32_e32 v44, v44, v195
	v_max_f32_e32 v242, v241, v209
	v_max_f32_e32 v213, v46, v210
	v_min_f32_e32 v245, v244, v219
	v_min_f32_e32 v182, v181, v220
	v_min_f32_e32 v209, v241, v209
	v_min_f32_e32 v46, v46, v210
	v_max_f32_e32 v219, v244, v219
	v_max_f32_e32 v181, v181, v220
	v_max_f32_e32 v59, v58, v57
	v_min_f32_e32 v57, v58, v57
	v_max_f32_e32 v236, v235, v212
	v_max_f32_e32 v195, v190, v44
	v_min_f32_e32 v212, v235, v212
	v_min_f32_e32 v44, v190, v44
	v_max_f32_e32 v243, v242, v213
	v_min_f32_e32 v246, v245, v182
	v_max_f32_e32 v210, v209, v46
	v_min_f32_e32 v220, v219, v181
	v_min_f32_e32 v213, v242, v213
	v_max_f32_e32 v182, v245, v182
	v_min_f32_e32 v46, v209, v46
	v_max_f32_e32 v181, v219, v181
	v_max_f32_e32 v237, v236, v178
	v_max_f32_e32 v234, v195, v179
	v_max_f32_e32 v235, v212, v50
	v_max_f32_e32 v190, v44, v180
	v_min_f32_e32 v247, v243, v246
	v_min_f32_e32 v241, v210, v220
	v_min_f32_e32 v242, v213, v182
	v_min_f32_e32 v209, v46, v181
	v_min_f32_e32 v178, v236, v178
	v_min_f32_e32 v179, v195, v179
	v_min_f32_e32 v50, v212, v50
	v_min_f32_e32 v44, v44, v180
	v_max_f32_e32 v236, v243, v246
	v_max_f32_e32 v210, v210, v220
	v_max_f32_e32 v182, v213, v182
	v_max_f32_e32 v46, v46, v181
	v_max_f32_e32 v223, v222, v183
	v_max_f32_e32 v224, v211, v48
	v_min_f32_e32 v183, v222, v183
	v_min_f32_e32 v48, v211, v48
	v_max_f32_e32 v238, v237, v234
	v_max_f32_e32 v239, v235, v190
	v_min_f32_e32 v244, v247, v241
	v_min_f32_e32 v219, v242, v209
	v_max_f32_e32 v195, v178, v179
	v_max_f32_e32 v180, v50, v44
	v_min_f32_e32 v220, v236, v210
	v_min_f32_e32 v181, v182, v46
	v_min_f32_e32 v234, v237, v234
	v_min_f32_e32 v190, v235, v190
	v_max_f32_e32 v237, v247, v241
	v_max_f32_e32 v209, v242, v209
	v_min_f32_e32 v178, v178, v179
	v_min_f32_e32 v44, v50, v44
	v_max_f32_e32 v50, v236, v210
	v_max_f32_e32 v46, v182, v46
	v_max_f32_e32 v225, v223, v224
	v_max_f32_e32 v211, v183, v48
	v_min_f32_e32 v223, v223, v224
	v_min_f32_e32 v48, v183, v48
	v_max_f32_e32 v240, v238, v239
	v_min_f32_e32 v245, v244, v219
	v_max_f32_e32 v212, v195, v180
	v_min_f32_e32 v213, v220, v181
	v_max_f32_e32 v235, v234, v190
	v_min_f32_e32 v241, v237, v209
	v_max_f32_e32 v179, v178, v44
	v_min_f32_e32 v182, v50, v46
	v_min_f32_e32 v238, v238, v239
	v_max_f32_e32 v219, v244, v219
	v_min_f32_e32 v180, v195, v180
	v_max_f32_e32 v181, v220, v181
	v_min_f32_e32 v190, v234, v190
	v_max_f32_e32 v209, v237, v209
	v_min_f32_e32 v44, v178, v44
	v_max_f32_e32 v46, v50, v46
	v_max_f32_e32 v226, v225, v51
	v_max_f32_e32 v221, v59, v173
	v_max_f32_e32 v222, v211, v60
	v_max_f32_e32 v56, v49, v61
	v_max_f32_e32 v224, v223, v62
	v_max_f32_e32 v58, v57, v63
	v_max_f32_e32 v183, v48, v52
	v_max_f32_e32 v55, v34, v53
	v_min_f32_e32 v248, v240, v245
	v_min_f32_e32 v243, v212, v213
	v_min_f32_e32 v242, v235, v241
	v_min_f32_e32 v210, v179, v182
	v_min_f32_e32 v239, v238, v219
	v_min_f32_e32 v195, v180, v181
	v_min_f32_e32 v234, v190, v209
	v_min_f32_e32 v178, v44, v46
	v_max_f32_e32 v227, v226, v221
	v_max_f32_e32 v228, v222, v56
	v_max_f32_e32 v230, v224, v58
	v_max_f32_e32 v231, v183, v55
	v_min_f32_e32 v246, v248, v243
	v_min_f32_e32 v236, v242, v210
	v_min_f32_e32 v220, v239, v195
	v_min_f32_e32 v237, v234, v178
	v_max_f32_e32 v229, v227, v228
	v_max_f32_e32 v232, v230, v231
	v_min_f32_e32 v247, v246, v236
	v_min_f32_e32 v244, v220, v237
	v_min_f32_e32 v51, v225, v51
	v_min_f32_e32 v59, v59, v173
	v_min_f32_e32 v60, v211, v60
	v_min_f32_e32 v61, v49, v61
	v_min_f32_e32 v62, v223, v62
	v_min_f32_e32 v57, v57, v63
	v_min_f32_e32 v48, v48, v52
	v_min_f32_e32 v34, v34, v53
	v_max_f32_e32 v63, v240, v245
	v_max_f32_e32 v212, v212, v213
	v_max_f32_e32 v235, v235, v241
	v_max_f32_e32 v179, v179, v182
	v_max_f32_e32 v219, v238, v219
	v_max_f32_e32 v180, v180, v181
	v_max_f32_e32 v190, v190, v209
	v_max_f32_e32 v44, v44, v46
	v_max_f32_e32 v233, v229, v232
	v_min_f32_e32 v50, v247, v244
	v_max_f32_e32 v173, v51, v59
	v_max_f32_e32 v211, v60, v61
	v_max_f32_e32 v223, v62, v57
	v_max_f32_e32 v53, v48, v34
	v_min_f32_e32 v213, v63, v212
	v_min_f32_e32 v182, v235, v179
	v_min_f32_e32 v181, v219, v180
	v_min_f32_e32 v46, v190, v44
	v_min_f32_e32 v227, v227, v228
	v_min_f32_e32 v228, v230, v231
	v_max_f32_e32 v230, v246, v236
	v_max_f32_e32 v220, v220, v237
	v_max_f32_e32 v50, v233, v50
	v_max_f32_e32 v44, v190, v44
	v_max_f32_e32 v225, v173, v211
	v_max_f32_e32 v233, v223, v53
	v_min_f32_e32 v240, v213, v182
	v_min_f32_e32 v209, v181, v46
	v_min_f32_e32 v221, v226, v221
	v_min_f32_e32 v222, v222, v56
	v_min_f32_e32 v224, v224, v58
	v_min_f32_e32 v183, v183, v55
	v_max_f32_e32 v241, v248, v243
	v_max_f32_e32 v210, v242, v210
	v_max_f32_e32 v195, v239, v195
	v_max_f32_e32 v234, v234, v178
	v_min_f32_e32 v51, v51, v59
	v_min_f32_e32 v59, v60, v61
	v_min_f32_e32 v57, v62, v57
	v_min_f32_e32 v34, v48, v34
	v_max_f32_e32 v60, v63, v212
	v_max_f32_e32 v62, v235, v179
	v_max_f32_e32 v58, v227, v228
	v_min_f32_e32 v63, v230, v220
	v_min_f32_e32 v211, v173, v211
	v_min_f32_e32 v223, v223, v53
	v_max_f32_e32 v213, v213, v182
	v_max_f32_e32 v46, v181, v46
	v_max_f32_e32 v226, v221, v222
	v_max_f32_e32 v238, v224, v183
	v_max_f32_e32 v243, v51, v59
	v_max_f32_e32 v245, v57, v34
	v_min_f32_e32 v179, v60, v62
	v_max_f32_e32 v63, v58, v63
	v_max_f32_e32 v53, v211, v223
	v_min_f32_e32 v58, v213, v46
	v_min_f32_e32 v181, v221, v222
	v_min_f32_e32 v221, v224, v183
	v_max_f32_e32 v222, v241, v210
	v_max_f32_e32 v224, v195, v234
	v_min_f32_e32 v51, v51, v59
	v_min_f32_e32 v59, v57, v34
	v_max_f32_e32 v231, v60, v62
	v_min_f32_e32 v57, v229, v232
	v_max_f32_e32 v62, v247, v244
	v_min_f32_e32 v239, v195, v234
	v_min_f32_e32 v242, v241, v210
	v_max_f32_e32 v212, v219, v180
	v_max_f32_e32 v178, v53, v58
	v_max_f32_e32 v53, v181, v221
	v_min_f32_e32 v173, v222, v224
	v_max_f32_e32 v183, v57, v62
	v_min_f32_e32 v57, v225, v233
	v_max_f32_e32 v62, v240, v209
	v_min_f32_e32 v219, v212, v44
	v_max_f32_e32 v180, v53, v173
	v_max_f32_e32 v190, v57, v62
	v_min_f32_e32 v57, v226, v238
	v_max_f32_e32 v173, v242, v239
	v_max_f32_e32 v55, v226, v238
	v_min_f32_e32 v56, v242, v239
	v_max_f32_e32 v210, v230, v220
	v_max_f32_e32 v195, v57, v173
	v_min_f32_e32 v57, v243, v245
	v_max_f32_e32 v173, v179, v219
	v_max_f32_e32 v55, v55, v56
	v_min_f32_e32 v56, v179, v219
	v_min_f32_e32 v179, v227, v228
	v_min_f32_e32 v52, v240, v209
	v_max_f32_e32 v209, v57, v173
	v_max_f32_e32 v46, v213, v46
	v_max_f32_e32 v44, v212, v44
	v_max_f32_e32 v210, v179, v210
	v_min_f32_e32 v179, v211, v223
	v_max_f32_e32 v211, v179, v46
	v_min_f32_e32 v46, v181, v221
	v_max_f32_e32 v181, v222, v224
	v_min_f32_e32 v53, v231, v44
	v_max_f32_e32 v44, v231, v44
	v_max_f32_e32 v212, v46, v181
	v_min_f32_e32 v46, v51, v59
	v_max_f32_e32 v34, v51, v59
	v_pk_add_f32 v[36:37], v[36:37], v[32:33] op_sel:[1,0] op_sel_hi:[0,1]
	v_mov_b32_e32 v37, 0xbf
	v_max_f32_e32 v213, v46, v44
	v_cmp_gt_i32_e32 vcc, 0, v36
	v_mov_b32_e32 v221, 0x50
	v_and_b32_e32 v41, 0xffffff00, v41
	v_cndmask_b32_e64 v37, v37, 64, vcc
	v_and_or_b32 v36, v36, s12, v37
	v_or_b32_e32 v217, v39, v41
	v_max_f32_e32 v49, v225, v233
	v_max_f32_e32 v44, v54, v36
	v_min_f32_e32 v54, v54, v36
	v_pk_add_f32 v[36:37], v[32:33], v[42:43] op_sel_hi:[0,1]
	v_cmp_gt_i32_e64 s[68:69], 0, v37
	v_mov_b32_e32 v42, 0x9f
	v_mov_b32_e32 v43, 0x60
	v_cndmask_b32_e64 v42, v42, v43, s[68:69]
	v_cmp_gt_i32_e64 s[68:69], 0, v36
	v_mov_b32_e32 v43, 0xaf
	v_and_b32_e32 v37, 0xffffff00, v37
	v_cndmask_b32_e64 v43, v43, v221, s[68:69]
	v_and_b32_e32 v36, 0xffffff00, v36
	v_or_b32_e32 v37, v42, v37
	v_or_b32_e32 v36, v43, v36
	v_min_f32_e32 v42, v37, v217
	v_max_f32_e32 v43, v36, v218
	v_max_f32_e32 v37, v37, v217
	v_min_f32_e32 v36, v36, v218
	v_max_f32_e32 v46, v44, v215
	v_max_f32_e32 v219, v54, v216
	v_min_f32_e32 v221, v43, v42
	v_min_f32_e32 v217, v36, v37
	v_max_f32_e32 v42, v43, v42
	v_max_f32_e32 v36, v36, v37
	v_max_f32_e32 v220, v46, v219
	v_min_f32_e32 v44, v44, v215
	v_min_f32_e32 v54, v54, v216
	v_min_f32_e32 v219, v46, v219
	v_mov_b32_e32 v46, v35
	v_min_f32_e32 v216, v42, v36
	v_max_f32_e32 v225, v42, v36
	v_pk_add_f32 v[36:37], v[32:33], v[46:47] op_sel_hi:[0,1]
	v_and_b32_e32 v45, 0xffffff80, v9
	v_max_f32_e32 v215, v44, v54
	v_min_f32_e32 v54, v44, v54
	v_mov_b32_e32 v44, v35
	v_cmp_gt_i32_e32 vcc, 0, v37
	v_mov_b32_e32 v35, 0x7f
	v_pk_add_f32 v[42:43], v[32:33], v[44:45] op_sel_hi:[0,1]
	v_cndmask_b32_e32 v35, v35, v196, vcc
	v_cmp_gt_i32_e32 vcc, 0, v36
	v_mov_b32_e32 v47, 0x8f
	v_mov_b32_e32 v45, 0x6f
	v_cndmask_b32_e32 v44, v47, v198, vcc
	v_cmp_gt_i32_e32 vcc, 0, v43
	v_mov_b32_e32 v46, 0x90
	v_and_b32_e32 v37, 0xffffff00, v37
	v_and_b32_e32 v36, 0xffffff00, v36
	v_cndmask_b32_e32 v45, v45, v46, vcc
	v_and_b32_e32 v43, 0xffffff00, v43
	v_cmp_gt_i32_e32 vcc, 0, v42
	v_or_b32_e32 v35, v35, v37
	v_or_b32_e32 v36, v44, v36
	v_or_b32_e32 v37, v45, v43
	v_and_b32_e32 v41, 0xffffff80, v10
	v_and_b32_e32 v40, 0xffffff80, v13
	v_cndmask_b32_e32 v46, v47, v198, vcc
	v_cmp_lt_f32_e32 vcc, v37, v35
	v_cmp_lt_f32_e64 s[8:9], v214, v36
	v_and_b32_e32 v39, 0xffffff80, v12
	v_cndmask_b32_e32 v43, v35, v37, vcc
	v_cndmask_b32_e64 v45, v36, v214, s[8:9]
	v_cndmask_b32_e32 v35, v37, v35, vcc
	v_pk_add_f32 v[36:37], v[32:33], v[40:41] op_sel_hi:[0,1]
	v_cmp_gt_i32_e64 s[80:81], 0, v37
	v_mov_b32_e32 v40, 0x5f
	v_mov_b32_e32 v41, 0xa0
	v_and_b32_e32 v38, 0xffffff80, v11
	v_cndmask_b32_e64 v40, v40, v41, s[80:81]
	v_and_b32_e32 v42, 0xffffff00, v42
	v_and_or_b32 v37, v37, s12, v40
	v_cmp_gt_i32_e64 s[80:81], 0, v36
	v_mov_b32_e32 v40, 0xd0
	v_pk_add_f32 v[38:39], v[32:33], v[38:39] op_sel_hi:[0,1]
	v_or_b32_e32 v42, v46, v42
	v_cndmask_b32_e64 v40, 47, v40, s[80:81]
	v_cmp_gt_i32_e64 s[80:81], 0, v39
	v_mov_b32_e32 v41, 0xc0
	v_cndmask_b32_e64 v42, v214, v42, s[8:9]
	v_cndmask_b32_e64 v41, 63, v41, s[80:81]
	v_cmp_gt_i32_e64 s[80:81], 0, v38
	v_mov_b32_e32 v214, 0x4f
	v_mov_b32_e32 v229, 0xb0
	v_cndmask_b32_e64 v214, v214, v229, s[80:81]
	v_and_b32_e32 v39, 0xffffff00, v39
	v_and_b32_e32 v38, 0xffffff00, v38
	v_and_b32_e32 v36, 0xffffff00, v36
	v_or_b32_e32 v39, v41, v39
	v_or_b32_e32 v38, v214, v38
	v_or_b32_e32 v36, v40, v36
	v_min_f32_e32 v40, v39, v36
	v_max_f32_e32 v41, v37, v38
	v_min_f32_e32 v37, v37, v38
	v_max_f32_e32 v36, v39, v36
	v_max_f32_e32 v44, v42, v43
	v_max_f32_e32 v46, v45, v35
	v_min_f32_e32 v214, v41, v40
	v_min_f32_e32 v38, v37, v36
	v_min_f32_e32 v42, v42, v43
	v_min_f32_e32 v35, v45, v35
	v_max_f32_e32 v40, v41, v40
	v_max_f32_e32 v36, v37, v36
	v_max_f32_e32 v47, v44, v46
	v_min_f32_e32 v39, v214, v38
	v_max_f32_e32 v43, v42, v35
	v_min_f32_e32 v37, v40, v36
	v_min_f32_e32 v44, v44, v46
	v_max_f32_e32 v38, v214, v38
	v_min_f32_e32 v35, v42, v35
	v_max_f32_e32 v36, v40, v36
	v_min_f32_e32 v218, v221, v217
	v_max_f32_e32 v217, v221, v217
	v_min_f32_e32 v229, v47, v39
	v_min_f32_e32 v41, v43, v37
	v_min_f32_e32 v46, v44, v38
	v_min_f32_e32 v40, v35, v36
	v_max_f32_e32 v39, v47, v39
	v_max_f32_e32 v37, v43, v37
	v_max_f32_e32 v38, v44, v38
	v_max_f32_e32 v35, v35, v36
	v_max_f32_e32 v222, v220, v218
	v_max_f32_e32 v223, v215, v216
	v_max_f32_e32 v221, v219, v217
	v_max_f32_e32 v226, v54, v225
	v_min_f32_e32 v218, v220, v218
	v_min_f32_e32 v215, v215, v216
	v_min_f32_e32 v217, v219, v217
	v_min_f32_e32 v54, v54, v225
	v_min_f32_e32 v43, v39, v37
	v_min_f32_e32 v36, v38, v35
	v_max_f32_e32 v37, v39, v37
	v_max_f32_e32 v35, v38, v35
	v_max_f32_e32 v216, v218, v215
	v_max_f32_e32 v219, v217, v54
	v_min_f32_e32 v44, v43, v36
	v_min_f32_e32 v215, v218, v215
	v_min_f32_e32 v54, v217, v54
	v_min_f32_e32 v38, v37, v35
	v_max_f32_e32 v43, v43, v36
	v_max_f32_e32 v35, v37, v35
	v_and_b32_e32 v37, 0xffffff80, v15
	v_mov_b32_e32 v36, v33
	v_pk_add_f32 v[32:33], v[32:33], v[36:37] op_sel_hi:[0,1]
	v_mov_b32_e32 v37, 0xe0
	v_max_f32_e32 v217, v215, v54
	v_min_f32_e32 v54, v215, v54
	v_cmp_gt_i32_e64 s[76:77], 0, v33
	v_and_b32_e32 v33, 0xffffff00, v33
	s_nop 0
	v_cndmask_b32_e64 v36, 15, v249, s[76:77]
	v_cmp_gt_i32_e64 s[76:77], 0, v32
	v_and_b32_e32 v32, 0xffffff00, v32
	v_or_b32_e32 v33, v36, v33
	v_cndmask_b32_e64 v37, 31, v37, s[76:77]
	v_or_b32_e32 v32, v37, v32
	v_max_f32_e32 v36, v32, v33
	v_min_f32_e32 v32, v32, v33
	v_max_f32_e32 v37, v36, v36
	v_max_f32_e32 v33, v32, v32
	v_max_f32_e32 v37, 0xff61b1e6, v37
	v_max_f32_e32 v33, 0xff61b1e6, v33
	v_max_f32_e32 v224, v222, v223
	v_max_f32_e32 v233, v37, v33
	v_min_f32_e32 v33, v37, v33
	v_max_f32_e32 v234, 0xff61b1e6, v233
	v_max_f32_e32 v37, 0xff61b1e6, v33
	v_cmp_nlt_f32_e32 vcc, s28, v33
	v_max_f32_e32 v227, v221, v226
	v_max_f32_e32 v235, v234, v37
	v_cmp_nlt_f32_e64 s[88:89], s28, v235
	v_cndmask_b32_e32 v33, v199, v33, vcc
	v_min_f32_e32 v45, v229, v41
	v_cndmask_b32_e64 v236, v199, v235, s[88:89]
	v_cmp_nlt_f32_e64 s[88:89], s28, v233
	v_min_f32_e32 v42, v46, v40
	v_min_f32_e32 v222, v222, v223
	v_cndmask_b32_e64 v233, v199, v233, s[88:89]
	v_cmp_nlt_f32_e64 s[88:89], s28, v36
	v_min_f32_e32 v221, v221, v226
	v_max_f32_e32 v41, v229, v41
	v_cndmask_b32_e64 v36, v199, v36, s[88:89]
	v_cmp_nlt_f32_e64 s[88:89], s28, v32
	v_max_f32_e32 v40, v46, v40
	s_nop 0
	v_cndmask_b32_e64 v32, v199, v32, s[88:89]
	v_max_f32_e32 v237, v36, v32
	v_min_f32_e32 v32, v36, v32
	v_max_f32_e32 v238, v233, v237
	v_max_f32_e32 v36, v33, v32
	v_max_f32_e32 v228, v224, v227
	v_min_f32_e32 v214, v45, v42
	v_max_f32_e32 v220, v216, v219
	v_max_f32_e32 v223, v222, v221
	v_min_f32_e32 v46, v41, v40
	v_min_f32_e32 v224, v224, v227
	v_max_f32_e32 v42, v45, v42
	v_min_f32_e32 v216, v216, v219
	v_min_f32_e32 v221, v222, v221
	v_max_f32_e32 v40, v41, v40
	v_max_f32_e32 v239, v238, v36
	v_min_f32_e32 v233, v233, v237
	v_min_f32_e32 v32, v33, v32
	v_min_f32_e32 v37, v234, v37
	v_min_f32_e32 v36, v238, v36
	v_max_f32_e32 v52, v49, v52
	s_mov_b64 s[6:7], s[96:97]
	v_cmp_nlt_f32_e64 s[88:89], s28, v239
	v_cmp_nlt_f32_e64 s[76:77], s28, v37
	v_cmp_nlt_f32_e64 s[14:15], s28, v36
	v_max_f32_e32 v230, v228, v214
	v_max_f32_e32 v47, v220, v44
	v_max_f32_e32 v226, v223, v46
	v_max_f32_e32 v39, v217, v38
	v_max_f32_e32 v45, v224, v42
	v_max_f32_e32 v219, v216, v43
	v_max_f32_e32 v41, v221, v40
	v_max_f32_e32 v215, v54, v35
	v_cndmask_b32_e64 v240, v199, v239, s[88:89]
	v_max_f32_e32 v33, v233, v32
	v_cndmask_b32_e64 v234, v199, v37, s[76:77]
	v_cndmask_b32_e64 v238, v199, v36, s[14:15]
	v_min_f32_e32 v32, v233, v32
	v_cmp_nlt_f32_e64 s[88:89], s28, v33
	v_cmp_nlt_f32_e32 vcc, s28, v32
	v_max_f32_e32 v48, v243, v245
	v_max_f32_e32 v225, v230, v47
	v_max_f32_e32 v218, v226, v39
	v_max_f32_e32 v227, v45, v219
	v_max_f32_e32 v222, v41, v215
	v_min_f32_e32 v241, v236, v240
	v_cndmask_b32_e64 v237, v199, v33, s[88:89]
	v_min_f32_e32 v243, v234, v238
	v_cndmask_b32_e32 v233, v199, v32, vcc
	v_max_f32_e32 v229, v225, v218
	v_max_f32_e32 v231, v227, v222
	v_min_f32_e32 v242, v241, v237
	v_min_f32_e32 v244, v243, v233
	v_min_f32_e32 v214, v228, v214
	v_max_f32_e32 v232, v229, v231
	v_min_f32_e32 v245, v242, v244
	v_max_f32_e32 v228, 0xff61b1e6, v235
	v_max_f32_e32 v235, v239, v239
	v_max_f32_e32 v36, v36, v36
	v_min_f32_e32 v44, v220, v44
	v_min_f32_e32 v46, v223, v46
	v_min_f32_e32 v38, v217, v38
	v_min_f32_e32 v42, v224, v42
	v_min_f32_e32 v43, v216, v43
	v_min_f32_e32 v40, v221, v40
	v_min_f32_e32 v35, v54, v35
	v_max_f32_e32 v235, 0xff61b1e6, v235
	v_max_f32_e32 v33, v33, v33
	v_max_f32_e32 v37, 0xff61b1e6, v37
	v_max_f32_e32 v36, 0xff61b1e6, v36
	v_max_f32_e32 v32, v32, v32
	v_max_f32_e32 v232, v232, v245
	s_mov_b32 s36, s18
	v_max_f32_e32 v33, 0xff61b1e6, v33
	v_max_f32_e32 v32, 0xff61b1e6, v32
	v_max_f32_e32 v220, v214, v44
	v_max_f32_e32 v217, v46, v38
	v_max_f32_e32 v216, v42, v43
	v_max_f32_e32 v54, v40, v35
	v_min_f32_e32 v239, v228, v235
	v_min_f32_e32 v245, 0xff61b1e6, v33
	v_min_f32_e32 v247, v37, v36
	v_min_f32_e32 v248, 0xff61b1e6, v32
	v_max_f32_e32 v223, v220, v217
	v_max_f32_e32 v221, v216, v54
	v_min_f32_e32 v246, v239, v245
	v_min_f32_e32 v249, v247, v248
	v_min_f32_e32 v47, v230, v47
	v_max_f32_e32 v230, v236, v240
	v_cmp_ngt_f32_e64 s[16:17], s28, v237
	v_max_f32_e32 v234, v234, v238
	v_cmp_ngt_f32_e64 s[14:15], s28, v233
	v_min_f32_e32 v44, v214, v44
	v_min_f32_e32 v38, v46, v38
	v_min_f32_e32 v42, v42, v43
	v_min_f32_e32 v35, v40, v35
	v_max_f32_e32 v214, v228, v235
	v_max_f32_e32 v36, v37, v36
	v_max_f32_e32 v224, v223, v221
	v_min_f32_e32 v250, v246, v249
	v_min_f32_e32 v39, v226, v39
	v_min_f32_e32 v45, v45, v219
	v_min_f32_e32 v41, v41, v215
	v_cndmask_b32_e64 v236, v199, v237, s[16:17]
	v_cndmask_b32_e64 v238, v199, v233, s[14:15]
	v_max_f32_e32 v46, v44, v38
	v_max_f32_e32 v40, v42, v35
	v_min_f32_e32 v228, v214, v33
	v_min_f32_e32 v37, v36, v32
	v_max_f32_e32 v224, v224, v250
	v_max_f32_e32 v226, v47, v39
	v_max_f32_e32 v215, v45, v41
	v_min_f32_e32 v240, v230, v236
	v_min_f32_e32 v250, v234, v238
	v_min_f32_e32 v218, v225, v218
	v_min_f32_e32 v222, v227, v222
	v_max_f32_e32 v237, v241, v237
	v_max_f32_e32 v233, v243, v233
	v_min_f32_e32 v39, v47, v39
	v_min_f32_e32 v41, v45, v41
	v_max_f32_e32 v47, v230, v236
	v_max_f32_e32 v230, v234, v238
	v_max_f32_e32 v43, v46, v40
	v_min_f32_e32 v235, v228, v37
	v_min_f32_e32 v217, v220, v217
	v_min_f32_e32 v54, v216, v54
	v_max_f32_e32 v239, v239, v245
	v_max_f32_e32 v243, v247, v248
	v_min_f32_e32 v38, v44, v38
	v_min_f32_e32 v35, v42, v35
	v_max_f32_e32 v33, v214, v33
	v_max_f32_e32 v32, v36, v32
	v_max_f32_e32 v219, v226, v215
	v_max_f32_e32 v227, v218, v222
	v_min_f32_e32 v241, v237, v233
	v_max_f32_e32 v45, v39, v41
	v_min_f32_e32 v234, v47, v230
	v_min_f32_e32 v229, v229, v231
	v_max_f32_e32 v231, v242, v244
	v_min_f32_e32 v215, v226, v215
	v_max_f32_e32 v226, v240, v250
	v_min_f32_e32 v251, v240, v250
	v_max_f32_e32 v43, v43, v235
	v_max_f32_e32 v216, v217, v54
	v_min_f32_e32 v245, v239, v243
	v_max_f32_e32 v42, v38, v35
	v_min_f32_e32 v36, v33, v32
	v_min_f32_e32 v221, v223, v221
	v_max_f32_e32 v223, v246, v249
	v_min_f32_e32 v40, v46, v40
	v_max_f32_e32 v37, v228, v37
	v_min_f32_e32 v218, v218, v222
	v_max_f32_e32 v222, v237, v233
	v_min_f32_e32 v54, v217, v54
	v_max_f32_e32 v217, v239, v243
	v_min_f32_e32 v39, v39, v41
	v_max_f32_e32 v41, v47, v230
	v_min_f32_e32 v35, v38, v35
	v_max_f32_e32 v32, v33, v32
	v_max_f32_e32 v227, v227, v241
	v_max_f32_e32 v45, v45, v234
	v_max_f32_e32 v229, v229, v231
	v_max_f32_e32 v215, v215, v226
	v_max_f32_e32 v61, v48, v56
	v_max_f32_e32 v182, v34, v53
	v_max_f32_e32 v219, v219, v251
	v_max_f32_e32 v216, v216, v245
	v_max_f32_e32 v36, v42, v36
	v_max_f32_e32 v221, v221, v223
	v_max_f32_e32 v37, v40, v37
	v_max_f32_e32 v218, v218, v222
	v_max_f32_e32 v217, v54, v217
	v_max_f32_e32 v39, v39, v41
	v_max_f32_e32 v32, v35, v32
	v_max_f32_e32 v49, v50, v52
	v_max_f32_e32 v56, v55, v61
	v_max_f32_e32 v58, v63, v178
	v_max_f32_e32 v60, v180, v182
	v_max_f32_e32 v62, v183, v190
	v_max_f32_e32 v173, v195, v209
	v_max_f32_e32 v179, v210, v211
	v_max_f32_e32 v181, v212, v213
	v_min_f32_e32 v225, v232, v224
	v_min_f32_e32 v241, v219, v43
	v_min_f32_e32 v245, v227, v216
	v_min_f32_e32 v42, v45, v36
	v_min_f32_e32 v223, v229, v221
	v_min_f32_e32 v40, v215, v37
	v_min_f32_e32 v222, v218, v217
	v_min_f32_e32 v33, v39, v32
	v_max_f32_e32 v48, v49, v56
	v_max_f32_e32 v53, v58, v60
	v_max_f32_e32 v57, v62, v173
	v_max_f32_e32 v59, v179, v181
	v_min_f32_e32 v220, v225, v241
	v_min_f32_e32 v44, v245, v42
	v_min_f32_e32 v46, v223, v40
	v_min_f32_e32 v35, v222, v33
	v_max_f32_e32 v34, v48, v53
	v_max_f32_e32 v51, v57, v59
	v_min_f32_e32 v214, v220, v44
	v_min_f32_e32 v38, v46, v35
	v_min_f32_e32 v47, v55, v61
	v_max_f32_e32 v235, v34, v51
	v_min_f32_e32 v41, v214, v38
	v_min_f32_e32 v61, v63, v178
	v_min_f32_e32 v63, v180, v182
	v_max_f32_e32 v54, v235, v41
	v_min_f32_e32 v41, v50, v52
	v_min_f32_e32 v182, v183, v190
	v_min_f32_e32 v183, v195, v209
	v_min_f32_e32 v190, v210, v211
	v_min_f32_e32 v209, v212, v213
	v_max_f32_e32 v212, v232, v224
	v_max_f32_e32 v43, v219, v43
	v_max_f32_e32 v216, v227, v216
	v_max_f32_e32 v36, v45, v36
	v_max_f32_e32 v221, v229, v221
	v_max_f32_e32 v37, v215, v37
	v_max_f32_e32 v217, v218, v217
	v_max_f32_e32 v32, v39, v32
	v_min_f32_e32 v49, v49, v56
	v_min_f32_e32 v224, v58, v60
	v_min_f32_e32 v62, v62, v173
	v_min_f32_e32 v173, v179, v181
	v_max_f32_e32 v181, v225, v241
	v_max_f32_e32 v42, v245, v42
	v_max_f32_e32 v40, v223, v40
	v_max_f32_e32 v33, v222, v33
	v_max_f32_e32 v50, v41, v47
	v_max_f32_e32 v178, v61, v63
	v_max_f32_e32 v195, v182, v183
	v_min_f32_e32 v213, v212, v43
	v_min_f32_e32 v45, v216, v36
	v_min_f32_e32 v215, v221, v37
	v_min_f32_e32 v39, v217, v32
	v_max_f32_e32 v226, v49, v224
	v_max_f32_e32 v179, v62, v173
	v_min_f32_e32 v225, v181, v42
	v_min_f32_e32 v222, v40, v33
	v_min_f32_e32 v41, v41, v47
	v_min_f32_e32 v47, v61, v63
	v_min_f32_e32 v63, v182, v183
	v_min_f32_e32 v182, v190, v209
	v_max_f32_e32 v43, v212, v43
	v_max_f32_e32 v36, v216, v36
	v_max_f32_e32 v37, v221, v37
	v_max_f32_e32 v32, v217, v32
	v_cmp_gt_f32_e64 s[24:25], v63, v182
	v_max_f32_e32 v210, v190, v209
	v_max_f32_e32 v56, v226, v179
	v_min_f32_e32 v58, v225, v222
	v_max_f32_e32 v223, v41, v47
	v_cndmask_b32_e64 v183, v182, v63, s[24:25]
	v_min_f32_e32 v209, v43, v36
	v_min_f32_e32 v212, v37, v32
	v_max_f32_e32 v56, v56, v58
	v_max_f32_e32 v58, v223, v183
	v_min_f32_e32 v60, v209, v212
	v_min_f32_e32 v48, v48, v53
	v_min_f32_e32 v217, v57, v59
	v_max_f32_e32 v44, v220, v44
	v_max_f32_e32 v35, v46, v35
	v_max_f32_e32 v58, v58, v60
	v_max_f32_e32 v53, v48, v217
	v_min_f32_e32 v46, v44, v35
	v_max_f32_e32 v180, v50, v178
	v_min_f32_e32 v219, v213, v45
	v_min_f32_e32 v218, v215, v39
	v_max_f32_e32 v59, v53, v46
	v_min_f32_e32 v46, v50, v178
	v_min_f32_e32 v50, v195, v210
	v_max_f32_e32 v45, v213, v45
	v_max_f32_e32 v39, v215, v39
	v_min_f32_e32 v49, v49, v224
	v_max_f32_e32 v53, v46, v50
	v_min_f32_e32 v57, v45, v39
	v_min_f32_e32 v213, v62, v173
	v_max_f32_e32 v42, v181, v42
	v_max_f32_e32 v33, v40, v33
	v_max_f32_e32 v60, v53, v57
	v_cmp_gt_f32_e64 s[20:21], v49, v213
	v_max_f32_e32 v211, v195, v210
	s_nop 0
	v_cndmask_b32_e64 v57, v213, v49, s[20:21]
	v_min_f32_e32 v40, v42, v33
	v_max_f32_e32 v36, v43, v36
	v_max_f32_e32 v32, v37, v32
	v_max_f32_e32 v61, v57, v40
	v_min_f32_e32 v40, v41, v47
	v_cndmask_b32_e64 v41, v63, v182, s[24:25]
	v_cmp_gt_f32_e64 s[14:15], v40, v41
	v_min_f32_e32 v34, v34, v51
	s_nop 0
	v_cndmask_b32_e64 v47, v41, v40, s[14:15]
	v_min_f32_e32 v37, v36, v32
	s_mov_b64 s[96:97], s[6:7]
	v_max_f32_e32 v62, v47, v37
	v_max_f32_e32 v37, v214, v38
	v_max_f32_e32 v35, v44, v35
	v_min_f32_e32 v55, v219, v218
	v_max_f32_e32 v63, v34, v37
	v_min_f32_e32 v34, v180, v211
	v_max_f32_e32 v37, v219, v218
	v_max_f32_e32 v52, v180, v211
	v_max_f32_e32 v33, v42, v33
	v_max_f32_e32 v173, v34, v37
	v_min_f32_e32 v34, v226, v179
	v_max_f32_e32 v37, v225, v222
	v_max_f32_e32 v32, v36, v32
	v_max_f32_e32 v178, v34, v37
	v_min_f32_e32 v34, v223, v183
	v_max_f32_e32 v37, v209, v212
	v_max_f32_e32 v55, v52, v55
	v_max_f32_e32 v179, v34, v37
	v_min_f32_e32 v34, v48, v217
	v_max_f32_e32 v180, v34, v35
	v_min_f32_e32 v34, v46, v50
	v_max_f32_e32 v35, v45, v39
	v_max_f32_e32 v181, v34, v35
	v_cndmask_b32_e64 v34, v49, v213, s[20:21]
	v_max_f32_e32 v182, v34, v33
	v_cndmask_b32_e64 v33, v40, v41, s[14:15]
	v_min_f32_e32 v52, v54, v55
	v_min_f32_e32 v190, v56, v58
	v_max_f32_e32 v183, v33, v32
	v_min_f32_e32 v53, v59, v60
	v_min_f32_e32 v57, v61, v62
	v_min_f32_e32 v195, v63, v173
	v_min_f32_e32 v209, v178, v179
	v_min_f32_e32 v210, v180, v181
	v_min_f32_e32 v211, v182, v183
	v_min_f32_e32 v216, v52, v190
	v_min_f32_e32 v215, v53, v57
	v_min_f32_e32 v51, v195, v209
	v_min_f32_e32 v50, v210, v211
	s_movk_i32 s10, 0xff
	v_min_f32_e32 v220, v216, v215
	v_min_f32_e32 v212, v51, v50
	s_movk_i32 s8, 0x7f
	v_bitop3_b32 v35, v31, s8, v31 bitop3:0xc
	v_min_f32_e32 v32, v220, v212
	v_and_b32_e32 v33, 0xff, v32
	v_bitop3_b32 v34, v32, s10, v32 bitop3:0xc
	v_cmp_gt_i32_e64 s[6:7], 0, v32
	v_readlane_b32 s94, v255, 39
	v_readlane_b32 s95, v255, 40
	v_cndmask_b32_e64 v213, v34, v33, s[6:7]
	v_and_b32_e32 v33, 0x7f, v31
	v_cmp_gt_i32_e64 s[6:7], 0, v31
	v_and_b32_e32 v34, 15, v213
	v_lshrrev_b32_e32 v214, 4, v213
	v_cndmask_b32_e64 v31, v35, v33, s[6:7]
	v_and_b32_e32 v33, 0x7f, v30
	v_bitop3_b32 v35, v30, s8, v30 bitop3:0xc
	v_cmp_gt_i32_e64 s[6:7], 0, v30
	v_readlane_b32 s86, v255, 31
	v_readlane_b32 s82, v255, 33
	v_cndmask_b32_e64 v30, v35, v33, s[6:7]
	v_and_b32_e32 v33, 0x7f, v29
	v_bitop3_b32 v35, v29, s8, v29 bitop3:0xc
	v_cmp_gt_i32_e64 s[6:7], 0, v29
	v_readlane_b32 s84, v255, 25
	v_readlane_b32 s87, v255, 32
	v_cndmask_b32_e64 v29, v35, v33, s[6:7]
	v_and_b32_e32 v33, 0x7f, v28
	v_bitop3_b32 v35, v28, s8, v28 bitop3:0xc
	v_cmp_gt_i32_e64 s[6:7], 0, v28
	v_readlane_b32 s92, v255, 35
	v_readlane_b32 s88, v255, 29
	v_cndmask_b32_e64 v28, v35, v33, s[6:7]
	v_and_b32_e32 v33, 0x7f, v27
	v_bitop3_b32 v35, v27, s8, v27 bitop3:0xc
	v_cmp_gt_i32_e64 s[6:7], 0, v27
	v_readlane_b32 s90, v255, 27
	v_readlane_b32 s78, v255, 13
	v_cndmask_b32_e64 v27, v35, v33, s[6:7]
	v_and_b32_e32 v33, 0x7f, v26
	v_bitop3_b32 v35, v26, s8, v26 bitop3:0xc
	v_cmp_gt_i32_e64 s[6:7], 0, v26
	v_readlane_b32 s83, v255, 34
	v_readlane_b32 s74, v255, 9
	v_cndmask_b32_e64 v26, v35, v33, s[6:7]
	v_and_b32_e32 v33, 0x7f, v25
	v_bitop3_b32 v35, v25, s8, v25 bitop3:0xc
	v_cmp_gt_i32_e64 s[6:7], 0, v25
	v_readlane_b32 s85, v255, 26
	v_readlane_b32 s76, v255, 11
	v_cndmask_b32_e64 v25, v35, v33, s[6:7]
	v_and_b32_e32 v33, 0x7f, v24
	v_bitop3_b32 v35, v24, s8, v24 bitop3:0xc
	v_cmp_gt_i32_e64 s[6:7], 0, v24
	v_readlane_b32 s22, v255, 23
	v_readlane_b32 s34, v255, 17
	v_cndmask_b32_e64 v24, v35, v33, s[6:7]
	v_and_b32_e32 v33, 0x7f, v23
	v_bitop3_b32 v35, v23, s8, v23 bitop3:0xc
	v_cmp_gt_i32_e64 s[6:7], 0, v23
	v_readlane_b32 s30, v255, 15
	v_readlane_b32 s81, v255, 41
	v_cndmask_b32_e64 v23, v35, v33, s[6:7]
	v_and_b32_e32 v33, 0x7f, v22
	v_bitop3_b32 v35, v22, s8, v22 bitop3:0xc
	v_cmp_gt_i32_e64 s[6:7], 0, v22
	s_movk_i32 s87, 0x4000
	v_readlane_b32 s93, v255, 36
	v_cndmask_b32_e64 v22, v35, v33, s[6:7]
	v_and_b32_e32 v33, 0x7f, v21
	v_bitop3_b32 v35, v21, s8, v21 bitop3:0xc
	v_cmp_gt_i32_e64 s[6:7], 0, v21
	v_readlane_b32 s89, v255, 30
	v_readlane_b32 s91, v255, 28
	v_cndmask_b32_e64 v21, v35, v33, s[6:7]
	v_and_b32_e32 v33, 0x7f, v20
	v_bitop3_b32 v35, v20, s8, v20 bitop3:0xc
	v_cmp_gt_i32_e64 s[6:7], 0, v20
	v_readlane_b32 s79, v255, 14
	v_readlane_b32 s83, v255, 37
	v_cndmask_b32_e64 v20, v35, v33, s[6:7]
	v_and_b32_e32 v33, 0x7f, v19
	v_bitop3_b32 v35, v19, s8, v19 bitop3:0xc
	v_cmp_gt_i32_e64 s[6:7], 0, v19
	v_readlane_b32 s75, v255, 10
	v_readlane_b32 s85, v255, 38
	v_cndmask_b32_e64 v19, v35, v33, s[6:7]
	v_and_b32_e32 v33, 0x7f, v18
	v_bitop3_b32 v35, v18, s8, v18 bitop3:0xc
	v_cmp_gt_i32_e64 s[6:7], 0, v18
	v_readlane_b32 s77, v255, 12
	v_readlane_b32 s23, v255, 24
	v_cndmask_b32_e64 v18, v35, v33, s[6:7]
	v_and_b32_e32 v33, 0x7f, v17
	v_bitop3_b32 v35, v17, s8, v17 bitop3:0xc
	v_cmp_gt_i32_e64 s[6:7], 0, v17
	s_mov_b32 s18, s36
	s_movk_i32 s27, 0x1200
	v_cndmask_b32_e64 v17, v35, v33, s[6:7]
	v_and_b32_e32 v33, 0x7f, v16
	v_bitop3_b32 v35, v16, s8, v16 bitop3:0xc
	v_cmp_gt_i32_e64 s[6:7], 0, v16
	v_readlane_b32 s35, v255, 18
	v_readlane_b32 s31, v255, 16
	v_cndmask_b32_e64 v33, v35, v33, s[6:7]
	v_lshl_add_u32 v252, v34, 8, v207
	ds_read_b32 v16, v252 offset:4096
	v_bitop3_b32 v35, v15, s8, v15 bitop3:0xc
	s_nop 0
	s_nop 1
	s_nop 1
	s_nop 1
	s_nop 1
	s_nop 1
	s_nop 1
	s_nop 1
	s_nop 1
	s_nop 1
	s_nop 1
	s_nop 1
	s_nop 1
	s_nop 1
	s_nop 1
	v_and_b32_e32 v34, 0x7f, v15
	s_nop 0
	s_waitcnt lgkmcnt(0)
	v_and_b32_e32 v252, 0x7f, v16
	v_cmp_gt_i32_e64 s[6:7], 0, v16
	v_xor_b32_e32 v16, 0x7f, v252
	s_nop 0
	v_cndmask_b32_e64 v16, v16, v252, s[6:7]
	v_cmp_gt_i32_e64 s[6:7], 0, v15
	v_and_b32_e32 v15, 0x7f, v14
	s_nop 0
	v_cndmask_b32_e64 v34, v35, v34, s[6:7]
	v_bitop3_b32 v35, v14, s8, v14 bitop3:0xc
	v_cmp_gt_i32_e64 s[6:7], 0, v14
	v_and_b32_e32 v14, 0x7f, v13
	s_nop 0
	v_cndmask_b32_e64 v35, v35, v15, s[6:7]
	v_bitop3_b32 v15, v13, s8, v13 bitop3:0xc
	v_cmp_gt_i32_e64 s[6:7], 0, v13
	v_and_b32_e32 v13, 0x7f, v12
	s_nop 0
	v_cndmask_b32_e64 v36, v15, v14, s[6:7]
	v_bitop3_b32 v14, v12, s8, v12 bitop3:0xc
	v_cmp_gt_i32_e64 s[6:7], 0, v12
	v_and_b32_e32 v12, 0x7f, v11
	v_max_f32_e32 v15, v59, v60
	v_cndmask_b32_e64 v37, v14, v13, s[6:7]
	v_bitop3_b32 v13, v11, s8, v11 bitop3:0xc
	v_cmp_gt_i32_e64 s[6:7], 0, v11
	v_and_b32_e32 v11, 0x7f, v10
	v_max_f32_e32 v14, v56, v58
	v_cndmask_b32_e64 v38, v13, v12, s[6:7]
	v_bitop3_b32 v12, v10, s8, v10 bitop3:0xc
	v_cmp_gt_i32_e64 s[6:7], 0, v10
	v_and_b32_e32 v10, 0x7f, v9
	v_max_f32_e32 v59, v61, v62
	v_cndmask_b32_e64 v39, v12, v11, s[6:7]
	v_bitop3_b32 v11, v9, s8, v9 bitop3:0xc
	v_cmp_gt_i32_e64 s[6:7], 0, v9
	v_and_b32_e32 v9, 0x7f, v8
	v_max_f32_e32 v60, v63, v173
	v_cndmask_b32_e64 v40, v11, v10, s[6:7]
	v_bitop3_b32 v10, v8, s8, v8 bitop3:0xc
	v_cmp_gt_i32_e64 s[6:7], 0, v8
	v_and_b32_e32 v8, 0x7f, v7
	v_max_f32_e32 v61, v178, v179
	v_cndmask_b32_e64 v41, v10, v9, s[6:7]
	v_bitop3_b32 v9, v7, s8, v7 bitop3:0xc
	v_cmp_gt_i32_e64 s[6:7], 0, v7
	v_and_b32_e32 v7, 0x7f, v6
	v_max_f32_e32 v62, v180, v181
	v_cndmask_b32_e64 v42, v9, v8, s[6:7]
	v_bitop3_b32 v8, v6, s8, v6 bitop3:0xc
	v_cmp_gt_i32_e64 s[6:7], 0, v6
	v_and_b32_e32 v6, 0x7f, v5
	v_max_f32_e32 v9, v210, v211
	v_cndmask_b32_e64 v43, v8, v7, s[6:7]
	v_bitop3_b32 v7, v5, s8, v5 bitop3:0xc
	v_cmp_gt_i32_e64 s[6:7], 0, v5
	v_and_b32_e32 v5, 0x7f, v4
	v_max_f32_e32 v8, v195, v209
	v_cndmask_b32_e64 v44, v7, v6, s[6:7]
	v_bitop3_b32 v6, v4, s8, v4 bitop3:0xc
	v_cmp_gt_i32_e64 s[6:7], 0, v4
	v_and_b32_e32 v4, 0x7f, v3
	v_max_f32_e32 v63, v182, v183
	v_cndmask_b32_e64 v45, v6, v5, s[6:7]
	v_bitop3_b32 v5, v3, s8, v3 bitop3:0xc
	v_cmp_gt_i32_e64 s[6:7], 0, v3
	v_and_b32_e32 v3, 0x7f, v2
	s_nop 0
	v_cndmask_b32_e64 v46, v5, v4, s[6:7]
	v_bitop3_b32 v4, v2, s8, v2 bitop3:0xc
	v_cmp_gt_i32_e64 s[6:7], 0, v2
	v_and_b32_e32 v2, 0x7f, v1
	s_nop 0
	v_cndmask_b32_e64 v47, v4, v3, s[6:7]
	v_bitop3_b32 v3, v1, s8, v1 bitop3:0xc
	v_cmp_gt_i32_e64 s[6:7], 0, v1
	v_and_b32_e32 v1, 0x7f, v0
	v_max_f32_e32 v4, v51, v50
	v_cndmask_b32_e64 v48, v3, v2, s[6:7]
	v_bitop3_b32 v2, v0, s8, v0 bitop3:0xc
	v_cmp_gt_i32_e64 s[6:7], 0, v0
	v_min_f32_e32 v56, v60, v61
	s_nop 0
	v_cndmask_b32_e64 v49, v2, v1, s[6:7]
	v_lshl_add_u32 v252, v214, 8, v207
	ds_read_b32 v0, v252
	v_min_f32_e32 v58, v62, v63
	s_nop 0
	v_max_f32_e32 v60, v60, v61
	v_max_f32_e32 v61, v62, v63
	v_readlane_b32 s46, v255, 21
	v_readlane_b32 s44, v255, 19
	v_readlane_b32 s47, v255, 22
	v_readlane_b32 s45, v255, 20
	s_nop 1
	s_nop 1
	s_nop 1
	s_nop 1
	s_nop 1
	s_nop 1
	s_nop 1
	s_nop 1
	s_nop 1
	s_nop 1
	s_nop 1
	s_nop 1
	s_waitcnt lgkmcnt(0)
	v_and_b32_e32 v252, 0x7f, v0
	v_cmp_gt_i32_e64 s[6:7], 0, v0
	v_xor_b32_e32 v0, 0x7f, v252
	s_nop 0
	v_cndmask_b32_e64 v3, v0, v252, s[6:7]
	v_max_f32_e32 v0, v220, v212
	v_and_b32_e32 v1, 0xff, v0
	v_bitop3_b32 v2, v0, s10, v0 bitop3:0xc
	v_cmp_gt_i32_e64 s[6:7], 0, v0
	v_and_b32_e32 v12, 0xffffff00, v0
	v_lshl_add_u32 v3, v3, 7, v16
	v_cndmask_b32_e64 v0, v2, v1, s[6:7]
	v_lshrrev_b32_e32 v1, 4, v0
	v_lshl_add_u32 v252, v1, 8, v207
	ds_read_b32 v2, v252
	v_and_b32_e32 v0, 15, v0
	s_nop 0
	s_nop 1
	s_nop 1
	s_nop 1
	s_nop 1
	s_nop 1
	s_nop 1
	s_nop 1
	s_nop 1
	s_nop 1
	s_nop 1
	s_nop 1
	s_nop 1
	s_nop 1
	s_nop 1
	s_nop 1
	s_waitcnt lgkmcnt(0)
	v_and_b32_e32 v252, 0x7f, v2
	v_cmp_gt_i32_e64 s[6:7], 0, v2
	v_xor_b32_e32 v2, 0x7f, v252
	s_nop 0
	v_cndmask_b32_e64 v1, v2, v252, s[6:7]
	v_lshl_add_u32 v252, v0, 8, v207
	ds_read_b32 v2, v252 offset:4096
	s_nop 1
	s_nop 1
	s_nop 1
	s_nop 1
	s_nop 1
	s_nop 1
	s_nop 1
	s_nop 1
	s_nop 1
	s_nop 1
	s_nop 1
	s_nop 1
	s_nop 1
	s_nop 1
	s_nop 1
	s_nop 1
	s_waitcnt lgkmcnt(0)
	v_and_b32_e32 v252, 0x7f, v2
	v_cmp_gt_i32_e64 s[6:7], 0, v2
	v_xor_b32_e32 v2, 0x7f, v252
	s_nop 0
	v_cndmask_b32_e64 v0, v2, v252, s[6:7]
	v_lshl_add_u32 v2, v1, 7, v0
	v_max_f32_e32 v0, v216, v215
	v_min_f32_e32 v1, v0, v4
	v_and_b32_e32 v5, 0xff, v1
	v_bitop3_b32 v6, v1, s10, v1 bitop3:0xc
	v_cmp_gt_i32_e64 s[8:9], 0, v1
	v_and_b32_e32 v50, 0xffffff00, v1
	v_max_f32_e32 v0, v0, v4
	v_cndmask_b32_e64 v1, v6, v5, s[8:9]
	v_lshrrev_b32_e32 v5, 4, v1
	v_lshl_add_u32 v252, v5, 8, v207
	ds_read_b32 v6, v252
	v_and_b32_e32 v1, 15, v1
	v_and_b32_e32 v4, 0xff, v0
	v_cmp_gt_i32_e64 s[6:7], 0, v0
	v_and_b32_e32 v51, 0xffffff00, v0
	s_nop 1
	s_nop 1
	s_nop 1
	s_nop 1
	s_nop 1
	s_nop 1
	s_nop 1
	s_nop 1
	s_nop 1
	s_nop 1
	s_nop 1
	s_nop 1
	s_nop 1
	s_nop 1
	s_waitcnt lgkmcnt(0)
	v_and_b32_e32 v252, 0x7f, v6
	v_cmp_gt_i32_e64 s[8:9], 0, v6
	v_xor_b32_e32 v6, 0x7f, v252
	s_nop 0
	v_cndmask_b32_e64 v5, v6, v252, s[8:9]
	v_lshl_add_u32 v252, v1, 8, v207
	ds_read_b32 v6, v252 offset:4096
	s_nop 1
	s_nop 1
	s_nop 1
	s_nop 1
	s_nop 1
	s_nop 1
	s_nop 1
	s_nop 1
	s_nop 1
	s_nop 1
	s_nop 1
	s_nop 1
	s_nop 1
	s_nop 1
	s_nop 1
	s_nop 1
	s_waitcnt lgkmcnt(0)
	v_and_b32_e32 v252, 0x7f, v6
	v_cmp_gt_i32_e64 s[8:9], 0, v6
	v_xor_b32_e32 v6, 0x7f, v252
	s_nop 0
	v_cndmask_b32_e64 v1, v6, v252, s[8:9]
	v_lshl_add_u32 v1, v5, 7, v1
	v_bitop3_b32 v5, v0, s10, v0 bitop3:0xc
	v_cndmask_b32_e64 v0, v5, v4, s[6:7]
	v_lshrrev_b32_e32 v4, 4, v0
	v_lshl_add_u32 v252, v4, 8, v207
	ds_read_b32 v5, v252
	v_and_b32_e32 v0, 15, v0
	s_nop 0
	s_nop 1
	s_nop 1
	s_nop 1
	s_nop 1
	s_nop 1
	s_nop 1
	s_nop 1
	s_nop 1
	s_nop 1
	s_nop 1
	s_nop 1
	s_nop 1
	s_nop 1
	s_nop 1
	s_nop 1
	s_waitcnt lgkmcnt(0)
	v_and_b32_e32 v252, 0x7f, v5
	v_cmp_gt_i32_e64 s[6:7], 0, v5
	v_xor_b32_e32 v5, 0x7f, v252
	s_nop 0
	v_cndmask_b32_e64 v4, v5, v252, s[6:7]
	v_lshl_add_u32 v252, v0, 8, v207
	ds_read_b32 v5, v252 offset:4096
	s_nop 1
	s_nop 1
	s_nop 1
	s_nop 1
	s_nop 1
	s_nop 1
	s_nop 1
	s_nop 1
	s_nop 1
	s_nop 1
	s_nop 1
	s_nop 1
	s_nop 1
	s_nop 1
	s_nop 1
	s_nop 1
	s_waitcnt lgkmcnt(0)
	v_and_b32_e32 v252, 0x7f, v5
	v_cmp_gt_i32_e64 s[6:7], 0, v5
	v_xor_b32_e32 v5, 0x7f, v252
	s_nop 0
	v_cndmask_b32_e64 v0, v5, v252, s[6:7]
	v_lshl_add_u32 v0, v4, 7, v0
	v_max_f32_e32 v4, v52, v190
	v_max_f32_e32 v5, v53, v57
	v_min_f32_e32 v6, v4, v5
	v_min_f32_e32 v10, v8, v9
	v_max_f32_e32 v4, v4, v5
	v_max_f32_e32 v8, v8, v9
	v_min_f32_e32 v7, v6, v10
	v_and_b32_e32 v11, 0xff, v7
	v_bitop3_b32 v13, v7, s10, v7 bitop3:0xc
	v_cmp_gt_i32_e64 s[8:9], 0, v7
	v_and_b32_e32 v52, 0xffffff00, v7
	v_max_f32_e32 v6, v6, v10
	v_cndmask_b32_e64 v7, v13, v11, s[8:9]
	v_lshrrev_b32_e32 v11, 4, v7
	v_lshl_add_u32 v252, v11, 8, v207
	ds_read_b32 v13, v252
	v_and_b32_e32 v7, 15, v7
	v_and_b32_e32 v10, 0xff, v6
	v_cmp_gt_i32_e64 s[6:7], 0, v6
	v_and_b32_e32 v53, 0xffffff00, v6
	s_nop 1
	s_nop 1
	s_nop 1
	s_nop 1
	s_nop 1
	s_nop 1
	s_nop 1
	s_nop 1
	s_nop 1
	s_nop 1
	s_nop 1
	s_nop 1
	s_nop 1
	s_nop 1
	s_waitcnt lgkmcnt(0)
	v_and_b32_e32 v252, 0x7f, v13
	v_cmp_gt_i32_e64 s[8:9], 0, v13
	v_xor_b32_e32 v13, 0x7f, v252
	s_nop 0
	v_cndmask_b32_e64 v11, v13, v252, s[8:9]
	v_lshl_add_u32 v252, v7, 8, v207
	ds_read_b32 v13, v252 offset:4096
	s_nop 1
	s_nop 1
	s_nop 1
	s_nop 1
	s_nop 1
	s_nop 1
	s_nop 1
	s_nop 1
	s_nop 1
	s_nop 1
	s_nop 1
	s_nop 1
	s_nop 1
	s_nop 1
	s_nop 1
	s_nop 1
	s_waitcnt lgkmcnt(0)
	v_and_b32_e32 v252, 0x7f, v13
	v_cmp_gt_i32_e64 s[8:9], 0, v13
	v_xor_b32_e32 v13, 0x7f, v252
	s_nop 0
	v_cndmask_b32_e64 v7, v13, v252, s[8:9]
	v_lshl_add_u32 v7, v11, 7, v7
	v_bitop3_b32 v11, v6, s10, v6 bitop3:0xc
	v_cndmask_b32_e64 v6, v11, v10, s[6:7]
	v_lshrrev_b32_e32 v10, 4, v6
	v_lshl_add_u32 v252, v10, 8, v207
	ds_read_b32 v11, v252
	v_and_b32_e32 v6, 15, v6
	v_max_f32_e32 v13, v54, v55
	v_min_f32_e32 v55, v56, v58
	s_nop 0
	v_max_f32_e32 v58, v56, v58
	s_nop 0
	s_nop 1
	s_nop 1
	s_nop 1
	s_nop 1
	s_nop 1
	s_nop 1
	s_nop 1
	s_nop 1
	s_nop 1
	s_nop 1
	s_nop 1
	s_nop 1
	s_nop 1
	s_waitcnt lgkmcnt(0)
	v_and_b32_e32 v252, 0x7f, v11
	v_cmp_gt_i32_e64 s[6:7], 0, v11
	v_xor_b32_e32 v11, 0x7f, v252
	s_nop 0
	v_cndmask_b32_e64 v10, v11, v252, s[6:7]
	v_lshl_add_u32 v252, v6, 8, v207
	ds_read_b32 v11, v252 offset:4096
	s_nop 1
	s_nop 1
	s_nop 1
	s_nop 1
	s_nop 1
	s_nop 1
	s_nop 1
	s_nop 1
	s_nop 1
	s_nop 1
	s_nop 1
	s_nop 1
	s_nop 1
	s_nop 1
	s_nop 1
	s_nop 1
	s_waitcnt lgkmcnt(0)
	v_and_b32_e32 v252, 0x7f, v11
	v_cmp_gt_i32_e64 s[6:7], 0, v11
	v_xor_b32_e32 v11, 0x7f, v252
	s_nop 0
	v_cndmask_b32_e64 v6, v11, v252, s[6:7]
	v_lshl_add_u32 v6, v10, 7, v6
	v_min_f32_e32 v5, v4, v8
	v_and_b32_e32 v9, 0xff, v5
	v_bitop3_b32 v10, v5, s10, v5 bitop3:0xc
	v_cmp_gt_i32_e64 s[8:9], 0, v5
	v_and_b32_e32 v57, 0xffffff00, v5
	v_max_f32_e32 v4, v4, v8
	v_cndmask_b32_e64 v5, v10, v9, s[8:9]
	v_lshrrev_b32_e32 v9, 4, v5
	v_lshl_add_u32 v252, v9, 8, v207
	ds_read_b32 v10, v252
	v_and_b32_e32 v5, 15, v5
	v_and_b32_e32 v8, 0xff, v4
	v_cmp_gt_i32_e64 s[6:7], 0, v4
	v_and_b32_e32 v209, 0xffffff00, v4
	s_nop 1
	s_nop 1
	s_nop 1
	s_nop 1
	s_nop 1
	s_nop 1
	s_nop 1
	s_nop 1
	s_nop 1
	s_nop 1
	s_nop 1
	s_nop 1
	s_nop 1
	s_nop 1
	s_waitcnt lgkmcnt(0)
	v_and_b32_e32 v252, 0x7f, v10
	v_cmp_gt_i32_e64 s[8:9], 0, v10
	v_xor_b32_e32 v10, 0x7f, v252
	s_nop 0
	v_cndmask_b32_e64 v9, v10, v252, s[8:9]
	v_lshl_add_u32 v252, v5, 8, v207
	ds_read_b32 v10, v252 offset:4096
	s_nop 1
	s_nop 1
	s_nop 1
	s_nop 1
	s_nop 1
	s_nop 1
	s_nop 1
	s_nop 1
	s_nop 1
	s_nop 1
	s_nop 1
	s_nop 1
	s_nop 1
	s_nop 1
	s_nop 1
	s_nop 1
	s_waitcnt lgkmcnt(0)
	v_and_b32_e32 v252, 0x7f, v10
	v_cmp_gt_i32_e64 s[8:9], 0, v10
	v_xor_b32_e32 v10, 0x7f, v252
	s_nop 0
	v_cndmask_b32_e64 v5, v10, v252, s[8:9]
	v_lshl_add_u32 v5, v9, 7, v5
	v_bitop3_b32 v9, v4, s10, v4 bitop3:0xc
	v_cndmask_b32_e64 v4, v9, v8, s[6:7]
	v_lshrrev_b32_e32 v8, 4, v4
	v_lshl_add_u32 v252, v8, 8, v207
	ds_read_b32 v9, v252
	v_and_b32_e32 v4, 15, v4
	s_nop 0
	s_nop 1
	s_nop 1
	s_nop 1
	s_nop 1
	s_nop 1
	s_nop 1
	s_nop 1
	s_nop 1
	s_nop 1
	s_nop 1
	s_nop 1
	s_nop 1
	s_nop 1
	s_nop 1
	s_nop 1
	s_waitcnt lgkmcnt(0)
	v_and_b32_e32 v252, 0x7f, v9
	v_cmp_gt_i32_e64 s[6:7], 0, v9
	v_xor_b32_e32 v9, 0x7f, v252
	s_nop 0
	v_cndmask_b32_e64 v8, v9, v252, s[6:7]
	v_lshl_add_u32 v252, v4, 8, v207
	ds_read_b32 v9, v252 offset:4096
	s_nop 1
	s_nop 1
	s_nop 1
	s_nop 1
	s_nop 1
	s_nop 1
	s_nop 1
	s_nop 1
	s_nop 1
	s_nop 1
	s_nop 1
	s_nop 1
	s_nop 1
	s_nop 1
	s_nop 1
	s_nop 1
	s_waitcnt lgkmcnt(0)
	v_and_b32_e32 v252, 0x7f, v9
	v_cmp_gt_i32_e64 s[6:7], 0, v9
	v_xor_b32_e32 v9, 0x7f, v252
	s_nop 0
	v_cndmask_b32_e64 v4, v9, v252, s[6:7]
	v_lshl_add_u32 v4, v8, 7, v4
	v_min_f32_e32 v8, v13, v14
	v_min_f32_e32 v9, v15, v59
	v_max_f32_e32 v13, v13, v14
	v_max_f32_e32 v59, v15, v59
	v_min_f32_e32 v10, v8, v9
	v_max_f32_e32 v8, v8, v9
	v_min_f32_e32 v11, v10, v55
	v_and_b32_e32 v173, 0xff, v11
	v_bitop3_b32 v178, v11, s10, v11 bitop3:0xc
	v_cmp_gt_i32_e64 s[8:9], 0, v11
	v_and_b32_e32 v54, 0xffffff00, v11
	v_max_f32_e32 v10, v10, v55
	v_cndmask_b32_e64 v11, v178, v173, s[8:9]
	v_lshrrev_b32_e32 v173, 4, v11
	v_lshl_add_u32 v252, v173, 8, v207
	ds_read_b32 v178, v252
	v_and_b32_e32 v11, 15, v11
	v_cmp_gt_i32_e64 s[6:7], 0, v10
	v_and_b32_e32 v55, 0xffffff00, v10
	s_nop 0
	v_min_f32_e32 v14, v13, v59
	v_min_f32_e32 v62, v60, v61
	v_max_f32_e32 v59, v13, v59
	v_max_f32_e32 v60, v60, v61
	s_nop 0
	s_nop 0
	v_min_f32_e32 v13, v59, v60
	v_and_b32_e32 v61, 0xffffff00, v13
	v_max_f32_e32 v59, v59, v60
	v_cmp_gt_i32_e32 vcc, 0, v59
	v_and_b32_e32 v60, 0xffffff00, v59
	v_sub_f32_e32 v12, v12, v60
	v_mul_f32_e32 v12, 0x3fb8aa3b, v12
	s_nop 0
	s_nop 1
	s_nop 1
	s_nop 1
	s_nop 1
	s_nop 1
	s_nop 1
	s_nop 1
	s_waitcnt lgkmcnt(0)
	v_and_b32_e32 v252, 0x7f, v178
	v_cmp_gt_i32_e64 s[8:9], 0, v178
	v_xor_b32_e32 v178, 0x7f, v252
	s_nop 0
	v_cndmask_b32_e64 v173, v178, v252, s[8:9]
	v_lshl_add_u32 v252, v11, 8, v207
	ds_read_b32 v178, v252 offset:4096
	s_nop 1
	s_nop 1
	s_nop 1
	s_nop 1
	s_nop 1
	s_nop 1
	s_nop 1
	s_nop 1
	s_nop 1
	s_nop 1
	s_nop 1
	s_nop 1
	s_nop 1
	s_nop 1
	s_nop 1
	s_nop 1
	s_waitcnt lgkmcnt(0)
	v_and_b32_e32 v252, 0x7f, v178
	v_cmp_gt_i32_e64 s[8:9], 0, v178
	v_xor_b32_e32 v178, 0x7f, v252
	s_nop 0
	v_cndmask_b32_e64 v11, v178, v252, s[8:9]
	v_lshl_add_u32 v11, v173, 7, v11
	v_and_b32_e32 v173, 0xff, v10
	v_bitop3_b32 v178, v10, s10, v10 bitop3:0xc
	v_cndmask_b32_e64 v10, v178, v173, s[6:7]
	v_lshrrev_b32_e32 v173, 4, v10
	v_lshl_add_u32 v252, v173, 8, v207
	ds_read_b32 v178, v252
	v_and_b32_e32 v10, 15, v10
	s_nop 0
	s_nop 1
	s_nop 1
	s_nop 1
	s_nop 1
	s_nop 1
	s_nop 1
	s_nop 1
	s_nop 1
	s_nop 1
	s_nop 1
	s_nop 1
	s_nop 1
	s_nop 1
	s_nop 1
	s_nop 1
	s_waitcnt lgkmcnt(0)
	v_and_b32_e32 v252, 0x7f, v178
	v_cmp_gt_i32_e64 s[6:7], 0, v178
	v_xor_b32_e32 v178, 0x7f, v252
	s_nop 0
	v_cndmask_b32_e64 v173, v178, v252, s[6:7]
	v_lshl_add_u32 v252, v10, 8, v207
	ds_read_b32 v178, v252 offset:4096
	s_nop 1
	s_nop 1
	s_nop 1
	s_nop 1
	s_nop 1
	s_nop 1
	s_nop 1
	s_nop 1
	s_nop 1
	s_nop 1
	s_nop 1
	s_nop 1
	s_nop 1
	s_nop 1
	s_nop 1
	s_nop 1
	s_waitcnt lgkmcnt(0)
	v_and_b32_e32 v252, 0x7f, v178
	v_cmp_gt_i32_e64 s[6:7], 0, v178
	v_xor_b32_e32 v178, 0x7f, v252
	s_nop 0
	v_cndmask_b32_e64 v10, v178, v252, s[6:7]
	v_lshl_add_u32 v10, v173, 7, v10
	v_min_f32_e32 v9, v8, v58
	v_and_b32_e32 v173, 0xff, v9
	v_bitop3_b32 v178, v9, s10, v9 bitop3:0xc
	v_cmp_gt_i32_e64 s[8:9], 0, v9
	v_and_b32_e32 v56, 0xffffff00, v9
	v_max_f32_e32 v8, v8, v58
	v_cndmask_b32_e64 v9, v178, v173, s[8:9]
	v_lshrrev_b32_e32 v173, 4, v9
	v_lshl_add_u32 v252, v173, 8, v207
	ds_read_b32 v178, v252
	v_and_b32_e32 v9, 15, v9
	v_cmp_gt_i32_e64 s[6:7], 0, v8
	v_and_b32_e32 v58, 0xffffff00, v8
	s_nop 0
	s_nop 1
	s_nop 1
	s_nop 1
	s_nop 1
	s_nop 1
	s_nop 1
	s_nop 1
	s_nop 1
	s_nop 1
	s_nop 1
	s_nop 1
	s_nop 1
	s_nop 1
	s_nop 1
	s_waitcnt lgkmcnt(0)
	v_and_b32_e32 v252, 0x7f, v178
	v_cmp_gt_i32_e64 s[8:9], 0, v178
	v_xor_b32_e32 v178, 0x7f, v252
	s_nop 0
	v_cndmask_b32_e64 v173, v178, v252, s[8:9]
	v_lshl_add_u32 v252, v9, 8, v207
	ds_read_b32 v178, v252 offset:4096
	s_nop 1
	s_nop 1
	s_nop 1
	s_nop 1
	s_nop 1
	s_nop 1
	s_nop 1
	s_nop 1
	s_nop 1
	s_nop 1
	s_nop 1
	s_nop 1
	s_nop 1
	s_nop 1
	s_nop 1
	s_nop 1
	s_waitcnt lgkmcnt(0)
	v_and_b32_e32 v252, 0x7f, v178
	v_cmp_gt_i32_e64 s[8:9], 0, v178
	v_xor_b32_e32 v178, 0x7f, v252
	s_nop 0
	v_cndmask_b32_e64 v9, v178, v252, s[8:9]
	v_lshl_add_u32 v9, v173, 7, v9
	v_and_b32_e32 v173, 0xff, v8
	v_bitop3_b32 v178, v8, s10, v8 bitop3:0xc
	v_cndmask_b32_e64 v8, v178, v173, s[6:7]
	v_lshrrev_b32_e32 v173, 4, v8
	v_lshl_add_u32 v252, v173, 8, v207
	ds_read_b32 v178, v252
	v_and_b32_e32 v8, 15, v8
	s_nop 0
	s_nop 1
	s_nop 1
	s_nop 1
	s_nop 1
	s_nop 1
	s_nop 1
	s_nop 1
	s_nop 1
	s_nop 1
	s_nop 1
	s_nop 1
	s_nop 1
	s_nop 1
	s_nop 1
	s_nop 1
	s_waitcnt lgkmcnt(0)
	v_and_b32_e32 v252, 0x7f, v178
	v_cmp_gt_i32_e64 s[6:7], 0, v178
	v_xor_b32_e32 v178, 0x7f, v252
	s_nop 0
	v_cndmask_b32_e64 v173, v178, v252, s[6:7]
	v_lshl_add_u32 v252, v8, 8, v207
	ds_read_b32 v178, v252 offset:4096
	s_nop 1
	s_nop 1
	s_nop 1
	s_nop 1
	s_nop 1
	s_nop 1
	s_nop 1
	s_nop 1
	s_nop 1
	s_nop 1
	s_nop 1
	s_nop 1
	s_nop 1
	s_nop 1
	s_nop 1
	s_nop 1
	s_waitcnt lgkmcnt(0)
	v_and_b32_e32 v252, 0x7f, v178
	v_cmp_gt_i32_e64 s[6:7], 0, v178
	v_xor_b32_e32 v178, 0x7f, v252
	s_nop 0
	v_cndmask_b32_e64 v8, v178, v252, s[6:7]
	v_lshl_add_u32 v8, v173, 7, v8
	v_min_f32_e32 v15, v14, v62
	v_and_b32_e32 v173, 0xff, v15
	v_bitop3_b32 v178, v15, s10, v15 bitop3:0xc
	v_cmp_gt_i32_e64 s[8:9], 0, v15
	v_and_b32_e32 v63, 0xffffff00, v15
	v_max_f32_e32 v14, v14, v62
	v_cndmask_b32_e64 v15, v178, v173, s[8:9]
	v_lshrrev_b32_e32 v173, 4, v15
	v_lshl_add_u32 v252, v173, 8, v207
	ds_read_b32 v178, v252
	v_and_b32_e32 v15, 15, v15
	v_cmp_gt_i32_e64 s[6:7], 0, v14
	v_and_b32_e32 v62, 0xffffff00, v14
	s_nop 0
	s_nop 1
	s_nop 1
	s_nop 1
	s_nop 1
	s_nop 1
	s_nop 1
	s_nop 1
	s_nop 1
	s_nop 1
	s_nop 1
	s_nop 1
	s_nop 1
	s_nop 1
	s_nop 1
	s_waitcnt lgkmcnt(0)
	v_and_b32_e32 v252, 0x7f, v178
	v_cmp_gt_i32_e64 s[8:9], 0, v178
	v_xor_b32_e32 v178, 0x7f, v252
	s_nop 0
	v_cndmask_b32_e64 v173, v178, v252, s[8:9]
	v_lshl_add_u32 v252, v15, 8, v207
	ds_read_b32 v178, v252 offset:4096
	s_nop 1
	s_nop 1
	s_nop 1
	s_nop 1
	s_nop 1
	s_nop 1
	s_nop 1
	s_nop 1
	s_nop 1
	s_nop 1
	s_nop 1
	s_nop 1
	s_nop 1
	s_nop 1
	s_nop 1
	s_nop 1
	s_waitcnt lgkmcnt(0)
	v_and_b32_e32 v252, 0x7f, v178
	v_cmp_gt_i32_e64 s[8:9], 0, v178
	v_xor_b32_e32 v178, 0x7f, v252
	s_nop 0
	v_cndmask_b32_e64 v15, v178, v252, s[8:9]
	v_lshl_add_u32 v15, v173, 7, v15
	v_and_b32_e32 v173, 0xff, v14
	v_bitop3_b32 v178, v14, s10, v14 bitop3:0xc
	v_cndmask_b32_e64 v14, v178, v173, s[6:7]
	v_lshrrev_b32_e32 v173, 4, v14
	v_lshl_add_u32 v252, v173, 8, v207
	ds_read_b32 v178, v252
	v_and_b32_e32 v14, 15, v14
	v_readlane_b32 s8, v253, 23
	v_readlane_b32 s9, v253, 24
	s_nop 0
	s_nop 1
	s_nop 1
	s_nop 1
	s_nop 1
	s_nop 1
	s_nop 1
	s_nop 1
	s_nop 1
	s_nop 1
	s_nop 1
	s_nop 1
	s_nop 1
	s_nop 1
	s_nop 1
	s_waitcnt lgkmcnt(0)
	v_and_b32_e32 v252, 0x7f, v178
	v_cmp_gt_i32_e64 s[6:7], 0, v178
	v_xor_b32_e32 v178, 0x7f, v252
	s_nop 0
	v_cndmask_b32_e64 v173, v178, v252, s[6:7]
	v_lshl_add_u32 v252, v14, 8, v207
	ds_read_b32 v178, v252 offset:4096
	s_nop 1
	s_nop 1
	s_nop 1
	s_nop 1
	s_nop 1
	s_nop 1
	s_nop 1
	s_nop 1
	s_nop 1
	s_nop 1
	s_nop 1
	s_nop 1
	s_nop 1
	s_nop 1
	s_nop 1
	s_nop 1
	s_waitcnt lgkmcnt(0)
	v_and_b32_e32 v252, 0x7f, v178
	v_cmp_gt_i32_e64 s[6:7], 0, v178
	v_xor_b32_e32 v178, 0x7f, v252
	s_nop 0
	v_cndmask_b32_e64 v14, v178, v252, s[6:7]
	v_lshl_add_u32 v14, v173, 7, v14
	v_and_b32_e32 v173, 0xff, v13
	v_bitop3_b32 v178, v13, s10, v13 bitop3:0xc
	v_cmp_gt_i32_e64 s[6:7], 0, v13
	s_nop 1
	v_cndmask_b32_e64 v13, v178, v173, s[6:7]
	v_lshrrev_b32_e32 v173, 4, v13
	v_lshl_add_u32 v252, v173, 8, v207
	ds_read_b32 v178, v252
	v_and_b32_e32 v13, 15, v13
	s_nop 0
	s_nop 1
	s_nop 1
	s_nop 1
	s_nop 1
	s_nop 1
	s_nop 1
	s_nop 1
	s_nop 1
	s_nop 1
	s_nop 1
	s_nop 1
	s_nop 1
	s_nop 1
	s_nop 1
	s_nop 1
	s_waitcnt lgkmcnt(0)
	v_and_b32_e32 v252, 0x7f, v178
	v_cmp_gt_i32_e64 s[6:7], 0, v178
	v_xor_b32_e32 v178, 0x7f, v252
	s_nop 0
	v_cndmask_b32_e64 v173, v178, v252, s[6:7]
	v_lshl_add_u32 v252, v13, 8, v207
	ds_read_b32 v178, v252 offset:4096
	s_nop 1
	s_nop 1
	s_nop 1
	s_nop 1
	s_nop 1
	s_nop 1
	s_nop 1
	s_nop 1
	s_nop 1
	s_nop 1
	s_nop 1
	s_nop 1
	s_nop 1
	s_nop 1
	s_nop 1
	s_nop 1
	s_waitcnt lgkmcnt(0)
	v_and_b32_e32 v252, 0x7f, v178
	v_cmp_gt_i32_e64 s[6:7], 0, v178
	v_xor_b32_e32 v178, 0x7f, v252
	s_nop 0
	v_cndmask_b32_e64 v13, v178, v252, s[6:7]
	v_lshl_add_u32 v13, v173, 7, v13
	v_and_b32_e32 v173, 0xff, v59
	v_bitop3_b32 v178, v59, s10, v59 bitop3:0xc
	v_cndmask_b32_e32 v59, v178, v173, vcc
	v_lshrrev_b32_e32 v173, 4, v59
	v_cmp_gt_u32_e32 vcc, 16, v59
	s_nop 1
	v_cndmask_b32_e32 v49, 0, v49, vcc
	v_cmp_eq_u32_e32 vcc, 1, v173
	s_nop 1
	v_cndmask_b32_e32 v48, v49, v48, vcc
	v_cmp_eq_u32_e32 vcc, 2, v173
	s_nop 1
	v_cndmask_b32_e32 v47, v48, v47, vcc
	v_cmp_eq_u32_e32 vcc, 3, v173
	s_nop 1
	v_cndmask_b32_e32 v46, v47, v46, vcc
	v_cmp_eq_u32_e32 vcc, 4, v173
	s_nop 1
	v_cndmask_b32_e32 v45, v46, v45, vcc
	v_cmp_eq_u32_e32 vcc, 5, v173
	s_nop 1
	v_cndmask_b32_e32 v44, v45, v44, vcc
	v_cmp_eq_u32_e32 vcc, 6, v173
	s_nop 1
	v_cndmask_b32_e32 v43, v44, v43, vcc
	v_cmp_eq_u32_e32 vcc, 7, v173
	s_nop 1
	v_cndmask_b32_e32 v42, v43, v42, vcc
	v_cmp_eq_u32_e32 vcc, 8, v173
	s_nop 1
	v_cndmask_b32_e32 v41, v42, v41, vcc
	v_cmp_eq_u32_e32 vcc, 9, v173
	s_nop 1
	v_cndmask_b32_e32 v40, v41, v40, vcc
	v_cmp_eq_u32_e32 vcc, 10, v173
	s_nop 1
	v_cndmask_b32_e32 v39, v40, v39, vcc
	v_cmp_eq_u32_e32 vcc, 11, v173
	s_nop 1
	v_cndmask_b32_e32 v38, v39, v38, vcc
	v_cmp_eq_u32_e32 vcc, 12, v173
	v_and_b32_e32 v39, 15, v59
	s_nop 0
	v_cndmask_b32_e32 v37, v38, v37, vcc
	v_cmp_eq_u32_e32 vcc, 13, v173
	s_nop 1
	v_cndmask_b32_e32 v36, v37, v36, vcc
	v_cmp_eq_u32_e32 vcc, 14, v173
	s_nop 1
	v_cndmask_b32_e32 v35, v36, v35, vcc
	v_cmp_eq_u32_e32 vcc, 15, v173
	v_exp_f32_e32 v36, v12
	v_and_b32_e32 v12, 0xffffff00, v32
	v_cndmask_b32_e32 v38, v35, v34, vcc
	v_cmp_eq_u32_e32 vcc, 0, v39
	v_sub_f32_e32 v12, v12, v60
	v_mul_f32_e32 v12, 0x3fb8aa3b, v12
	v_cndmask_b32_e32 v33, 0, v33, vcc
	v_cmp_eq_u32_e32 vcc, 1, v39
	v_exp_f32_e32 v37, v12
	s_nop 0
	v_cndmask_b32_e32 v17, v33, v17, vcc
	v_cmp_eq_u32_e32 vcc, 2, v39
	v_sub_f32_e32 v33, v51, v60
	v_mul_f32_e32 v33, 0x3fb8aa3b, v33
	v_cndmask_b32_e32 v17, v17, v18, vcc
	v_cmp_eq_u32_e32 vcc, 3, v39
	v_sub_f32_e32 v18, v60, v60
	v_mul_f32_e32 v18, 0x3fb8aa3b, v18
	v_cndmask_b32_e32 v17, v17, v19, vcc
	v_cmp_eq_u32_e32 vcc, 4, v39
	v_sub_f32_e32 v19, v61, v60
	v_exp_f32_e32 v18, v18
	v_cndmask_b32_e32 v17, v17, v20, vcc
	v_cmp_eq_u32_e32 vcc, 5, v39
	v_mul_f32_e32 v19, 0x3fb8aa3b, v19
	v_sub_f32_e32 v20, v62, v60
	v_cndmask_b32_e32 v17, v17, v21, vcc
	v_exp_f32_e32 v19, v19
	v_mul_f32_e32 v20, 0x3fb8aa3b, v20
	v_sub_f32_e32 v21, v63, v60
	v_cmp_eq_u32_e32 vcc, 6, v39
	v_exp_f32_e32 v20, v20
	v_mul_f32_e32 v21, 0x3fb8aa3b, v21
	v_cndmask_b32_e32 v17, v17, v22, vcc
	v_cmp_eq_u32_e32 vcc, 7, v39
	v_exp_f32_e32 v21, v21
	v_add_f32_e32 v22, 0, v18
	v_cndmask_b32_e32 v17, v17, v23, vcc
	v_cmp_eq_u32_e32 vcc, 8, v39
	v_add_f32_e32 v22, v19, v22
	v_add_f32_e32 v22, v20, v22
	v_cndmask_b32_e32 v17, v17, v24, vcc
	v_cmp_eq_u32_e32 vcc, 9, v39
	v_sub_f32_e32 v23, v56, v60
	v_mul_f32_e32 v23, 0x3fb8aa3b, v23
	v_cndmask_b32_e32 v17, v17, v25, vcc
	v_cmp_eq_u32_e32 vcc, 10, v39
	v_sub_f32_e32 v24, v55, v60
	v_exp_f32_e32 v23, v23
	v_cndmask_b32_e32 v17, v17, v26, vcc
	v_add_f32_e32 v26, v21, v22
	v_sub_f32_e32 v22, v58, v60
	v_mul_f32_e32 v22, 0x3fb8aa3b, v22
	v_exp_f32_e32 v22, v22
	v_mul_f32_e32 v24, 0x3fb8aa3b, v24
	v_sub_f32_e32 v25, v54, v60
	v_exp_f32_e32 v24, v24
	v_mul_f32_e32 v25, 0x3fb8aa3b, v25
	v_cmp_eq_u32_e32 vcc, 11, v39
	v_exp_f32_e32 v25, v25
	v_add_f32_e32 v26, v22, v26
	v_cndmask_b32_e32 v17, v17, v27, vcc
	v_cmp_eq_u32_e32 vcc, 12, v39
	v_add_f32_e32 v26, v23, v26
	v_add_f32_e32 v26, v24, v26
	v_cndmask_b32_e32 v17, v17, v28, vcc
	v_cmp_eq_u32_e32 vcc, 13, v39
	v_sub_f32_e32 v27, v57, v60
	v_mul_f32_e32 v27, 0x3fb8aa3b, v27
	v_cndmask_b32_e32 v17, v17, v29, vcc
	v_cmp_eq_u32_e32 vcc, 14, v39
	v_sub_f32_e32 v28, v53, v60
	v_exp_f32_e32 v27, v27
	v_cndmask_b32_e32 v17, v17, v30, vcc
	v_add_f32_e32 v30, v25, v26
	v_sub_f32_e32 v26, v209, v60
	v_mul_f32_e32 v26, 0x3fb8aa3b, v26
	v_exp_f32_e32 v26, v26
	v_mul_f32_e32 v28, 0x3fb8aa3b, v28
	v_sub_f32_e32 v29, v52, v60
	v_exp_f32_e32 v28, v28
	v_mul_f32_e32 v29, 0x3fb8aa3b, v29
	v_exp_f32_e32 v29, v29
	v_exp_f32_e32 v34, v33
	v_sub_f32_e32 v33, v50, v60
	v_add_f32_e32 v30, v26, v30
	v_mul_f32_e32 v33, 0x3fb8aa3b, v33
	v_add_f32_e32 v30, v27, v30
	v_exp_f32_e32 v35, v33
	v_add_f32_e32 v30, v28, v30
	v_add_f32_e32 v30, v29, v30
	v_add_f32_e32 v12, v34, v30
	v_add_f32_e32 v12, v35, v12
	v_add_f32_e32 v12, v36, v12
	v_add_f32_e32 v30, v37, v12
	v_div_scale_f32 v32, s[6:7], v30, v30, 1.0
	v_rcp_f32_e32 v33, v32
	v_cmp_eq_u32_e32 vcc, 15, v39
	v_readlane_b32 s6, v255, 46
	s_lshl_b32 s6, s6, 4
	v_cndmask_b32_e32 v12, v17, v31, vcc
	v_fma_f32 v17, -v32, v33, 1.0
	v_fmac_f32_e32 v33, v17, v33
	v_div_scale_f32 v17, vcc, 1.0, v30, 1.0
	v_mul_f32_e32 v31, v17, v33
	v_lshl_add_u32 v12, v38, 7, v12
	v_fma_f32 v38, -v32, v31, v17
	v_fmac_f32_e32 v31, v38, v33
	v_fma_f32 v17, -v32, v31, v17
	v_div_fmas_f32 v17, v17, v33, v31
	v_div_fixup_f32 v30, v17, v30, 1.0
	v_lshlrev_b64 v[16:17], 9, v[176:177]
	s_ashr_i32 s7, s6, 31
	v_lshl_add_u64 v[32:33], s[94:95], 0, v[16:17]
	s_lshl_b64 s[6:7], s[6:7], 2
	v_lshl_add_u64 v[32:33], v[32:33], 0, s[6:7]
	v_lshl_add_u64 v[16:17], s[8:9], 0, v[16:17]
	v_lshl_add_u64 v[16:17], v[16:17], 0, s[6:7]
	global_store_dwordx4 v[32:33], v[12:15], off
	v_readlane_b32 s8, v255, 44
	v_readlane_b32 s9, v255, 45
	v_pk_mul_f32 v[12:13], v[18:19], v[30:31] op_sel_hi:[1,0]
	v_pk_mul_f32 v[14:15], v[20:21], v[30:31] op_sel_hi:[1,0]
	global_store_dwordx4 v[16:17], v[12:15], off
	global_store_dwordx4 v[32:33], v[8:11], off offset:16
	s_nop 1
	v_pk_mul_f32 v[8:9], v[22:23], v[30:31] op_sel_hi:[1,0]
	v_pk_mul_f32 v[10:11], v[24:25], v[30:31] op_sel_hi:[1,0]
	global_store_dwordx4 v[16:17], v[8:11], off offset:16
	global_store_dwordx4 v[32:33], v[4:7], off offset:32
	s_nop 1
	v_pk_mul_f32 v[4:5], v[26:27], v[30:31] op_sel_hi:[1,0]
	v_pk_mul_f32 v[6:7], v[28:29], v[30:31] op_sel_hi:[1,0]
	global_store_dwordx4 v[16:17], v[4:7], off offset:32
	global_store_dwordx4 v[32:33], v[0:3], off offset:48
	s_nop 1
	v_pk_mul_f32 v[0:1], v[34:35], v[30:31] op_sel_hi:[1,0]
	v_pk_mul_f32 v[2:3], v[36:37], v[30:31] op_sel_hi:[1,0]
	global_store_dwordx4 v[16:17], v[0:3], off offset:48
	s_branch .LBB0_696
